# P6 router logits of experts 0-13 regenerated with v_pk_fma_f32 (f32 packed accumulators) and 6-deep LDS read pipeline
# speedup vs baseline: 1.0095x; 1.0095x over previous
.LBB0_2123:
	v_lshl_add_u64 v[28:29], s[44:45], 0, v[16:17]
	v_add_co_u32_e32 v4, vcc, 0x37a00000, v28
	s_add_i32 s0, s80, s8
	s_nop 0
	v_addc_co_u32_e32 v5, vcc, 0, v29, vcc
	global_load_dwordx2 v[62:63], v[4:5], off
	global_load_dwordx2 v[60:61], v[4:5], off offset:512
	global_load_dwordx2 v[48:49], v[4:5], off offset:1024
	s_waitcnt lgkmcnt(0)
	global_load_dwordx2 v[6:7], v[4:5], off offset:1536
	global_load_dwordx2 v[46:47], v[4:5], off offset:2048
	global_load_dwordx2 v[44:45], v[4:5], off offset:2560
	global_load_dwordx2 v[42:43], v[4:5], off offset:3072
	s_nop 0
	global_load_dwordx2 v[4:5], v[4:5], off offset:3584
	s_cmp_lt_i32 s0, s86
	s_cselect_b32 s48, s0, s8
	s_ashr_i32 s49, s48, 31
	s_lshl_b64 s[50:51], s[48:49], 12
	v_mov_b32_e32 v2, s81
	s_min_i32 s0, s8, 0x4000
	s_lshr_b32 s0, s0, 12
	s_mulk_i32 s0, 0x3000
	s_ashr_i32 s1, s0, 31
	s_lshl_b64 s[0:1], s[0:1], 2
	s_add_u32 s2, s6, s0
	s_addc_u32 s3, s7, s1
	s_min_i32 s0, s48, 0x4000
	s_lshr_b32 s0, s0, 12
	s_mulk_i32 s0, 0x3000
	s_ashr_i32 s1, s0, 31
	s_lshl_b64 s[0:1], s[0:1], 2
	s_add_u32 s0, s6, s0
	s_addc_u32 s1, s7, s1
	s_waitcnt vmcnt(7)
	v_and_b32_e32 v103, 0xffff0000, v63
	v_and_b32_e32 v101, 0xffff0000, v62
	v_lshlrev_b32_e32 v102, 16, v63
	s_waitcnt vmcnt(4)
	v_lshlrev_b32_e32 v25, 16, v6
	s_waitcnt vmcnt(0)
	v_lshlrev_b32_e32 v21, 16, v4
	v_and_b32_e32 v19, 0xffff0000, v4
	v_lshlrev_b32_e32 v58, 16, v5
	v_and_b32_e32 v59, 0xffff0000, v5
	v_lshl_add_u64 v[4:5], v[8:9], 0, s[50:51]
	v_and_b32_e32 v23, 0xffff0000, v6
	v_lshlrev_b32_e32 v26, 16, v7
	v_and_b32_e32 v27, 0xffff0000, v7
	global_load_dwordx2 v[40:41], v[4:5], off
	global_load_dwordx2 v[38:39], v[4:5], off offset:512
	global_load_dwordx2 v[36:37], v[4:5], off offset:1024
	global_load_dwordx2 v[6:7], v[4:5], off offset:1536
	global_load_dwordx2 v[34:35], v[4:5], off offset:2048
	global_load_dwordx2 v[32:33], v[4:5], off offset:2560
	global_load_dwordx2 v[30:31], v[4:5], off offset:3072
	global_load_dwordx2 v[50:51], v[4:5], off offset:3584
	ds_read_b64 v[64:65], v2
	v_mul_f32_e32 v2, v103, v103
	v_lshlrev_b32_e32 v100, 16, v62
	v_pk_fma_f32 v[62:63], v[102:103], v[102:103], v[2:3] op_sel_hi:[1,1,0]
	v_and_b32_e32 v99, 0xffff0000, v61
	v_and_b32_e32 v98, 0xffff0000, v60
	v_mul_f32_e32 v2, v101, v101
	v_lshlrev_b32_e32 v95, 16, v61
	v_lshlrev_b32_e32 v94, 16, v60
	v_pk_mul_f32 v[60:61], v[98:99], v[98:99]
	v_lshlrev_b32_e32 v90, 16, v48
	v_and_b32_e32 v91, 0xffff0000, v48
	v_lshlrev_b32_e32 v96, 16, v49
	v_and_b32_e32 v97, 0xffff0000, v49
	v_pk_fma_f32 v[48:49], v[100:101], v[100:101], v[2:3] op_sel_hi:[1,1,0]
	s_waitcnt lgkmcnt(0)
	v_readfirstlane_b32 s9, v64
	v_readfirstlane_b32 s12, v65
	v_pk_fma_f32 v[60:61], v[94:95], v[94:95], v[60:61]
	v_mov_b32_e32 v24, v48
	v_mov_b32_e32 v64, v62
	v_mov_b32_e32 v65, v25
	v_mul_f32_e32 v4, v23, v23
	v_pk_add_f32 v[48:49], v[48:49], v[62:63]
	v_pk_mul_f32 v[62:63], v[24:25], v[64:65]
	v_pk_add_f32 v[60:61], v[60:61], v[60:61] op_sel:[0,1] op_sel_hi:[1,0]
	v_mov_b32_e32 v49, v63
	v_mov_b32_e32 v61, v4
	v_mul_f32_e32 v2, v91, v91
	v_pk_add_f32 v[48:49], v[48:49], v[60:61]
	v_pk_fma_f32 v[60:61], v[90:91], v[90:91], v[2:3] op_sel_hi:[1,1,0]
	v_mul_f32_e32 v2, v97, v97
	v_mul_f32_e32 v18, v27, v27
	v_pk_fma_f32 v[62:63], v[96:97], v[96:97], v[2:3] op_sel_hi:[1,1,0]
	v_and_b32_e32 v107, 0xffff0000, v47
	v_mov_b32_e32 v63, v18
	v_and_b32_e32 v106, 0xffff0000, v46
	v_lshlrev_b32_e32 v105, 16, v47
	v_lshlrev_b32_e32 v104, 16, v46
	v_pk_mul_f32 v[46:47], v[106:107], v[106:107]
	v_and_b32_e32 v93, 0xffff0000, v45
	v_pk_fma_f32 v[46:47], v[104:105], v[104:105], v[46:47]
	v_and_b32_e32 v92, 0xffff0000, v44
	v_pk_add_f32 v[46:47], v[46:47], v[46:47] op_sel:[0,1] op_sel_hi:[1,0]
	v_lshlrev_b32_e32 v89, 16, v45
	v_lshlrev_b32_e32 v88, 16, v44
	v_pk_mul_f32 v[44:45], v[92:93], v[92:93]
	v_lshlrev_b32_e32 v78, 16, v42
	v_and_b32_e32 v79, 0xffff0000, v42
	v_lshlrev_b32_e32 v80, 16, v43
	v_and_b32_e32 v81, 0xffff0000, v43
	v_pk_fma_f32 v[44:45], v[88:89], v[88:89], v[44:45]
	v_mul_f32_e32 v2, v19, v19
	v_pk_add_f32 v[44:45], v[44:45], v[44:45] op_sel:[0,1] op_sel_hi:[1,0]
	s_add_u32 s52, s9, s46
	v_mov_b32_e32 v45, v2
	v_mul_f32_e32 v2, v79, v79
	s_addc_u32 s53, s12, s47
	s_add_u32 s58, s2, 0x6000
	v_mul_f32_e32 v4, v58, v58
	s_addc_u32 s59, s3, 0
	s_add_u32 s60, s2, 0x8000
	s_addc_u32 s61, s3, 0
	s_add_u32 s54, s0, 0x6000
	s_addc_u32 s55, s1, 0
	s_add_u32 s56, s0, 0x8000
	s_mov_b32 s0, 0x3a000000
	s_addc_u32 s57, s1, 0
	v_mov_b32_e32 v22, v25
	s_waitcnt vmcnt(7)
	v_and_b32_e32 v73, 0xffff0000, v41
	v_and_b32_e32 v71, 0xffff0000, v40
	v_lshlrev_b32_e32 v72, 16, v41
	s_waitcnt vmcnt(4)
	v_lshlrev_b32_e32 v55, 16, v6
	v_and_b32_e32 v53, 0xffff0000, v6
	v_mul_f32_e32 v6, v26, v26
	v_mov_b32_e32 v61, v6
	v_pk_add_f32 v[60:61], v[60:61], v[62:63]
	v_mul_f32_e32 v6, v59, v59
	v_pk_add_f32 v[48:49], v[48:49], v[60:61]
	v_lshlrev_b32_e32 v70, 16, v40
	v_pk_add_f32 v[42:43], v[48:49], v[48:49] op_sel:[0,1] op_sel_hi:[1,0]
	v_mov_b32_e32 v48, v46
	v_mov_b32_e32 v20, v42
	v_mov_b32_e32 v49, v21
	v_pk_add_f32 v[42:43], v[42:43], v[46:47]
	v_pk_mul_f32 v[46:47], v[20:21], v[48:49]
	v_and_b32_e32 v77, 0xffff0000, v39
	v_mov_b32_e32 v43, v47
	v_pk_add_f32 v[42:43], v[42:43], v[44:45]
	v_pk_fma_f32 v[44:45], v[78:79], v[78:79], v[2:3] op_sel_hi:[1,1,0]
	v_mul_f32_e32 v2, v81, v81
	v_pk_fma_f32 v[46:47], v[80:81], v[80:81], v[2:3] op_sel_hi:[1,1,0]
	v_mov_b32_e32 v45, v4
	v_mov_b32_e32 v47, v6
	v_pk_add_f32 v[44:45], v[44:45], v[46:47]
	v_mul_f32_e32 v2, v73, v73
	v_pk_add_f32 v[108:109], v[42:43], v[44:45]
	global_load_dwordx4 v[118:121], v181, s[52:53]
	global_load_dwordx4 v[122:125], v181, s[60:61]
	global_load_dwordx4 v[126:129], v181, s[58:59]
	global_load_dwordx4 v[130:133], v181, s[52:53] offset:1024
	global_load_dwordx4 v[134:137], v182, s[60:61]
	global_load_dwordx4 v[138:141], v182, s[58:59]
	global_load_dwordx4 v[142:145], v181, s[52:53] offset:2048
	global_load_dwordx4 v[146:149], v183, s[60:61]
	global_load_dwordx4 v[150:153], v183, s[58:59]
	global_load_dwordx4 v[154:157], v181, s[52:53] offset:3072
	global_load_dwordx4 v[158:161], v184, s[60:61]
	global_load_dwordx4 v[162:165], v184, s[58:59]
	global_load_dwordx4 v[166:169], v185, s[52:53]
	global_load_dwordx4 v[170:173], v185, s[60:61]
	global_load_dwordx4 v[174:177], v185, s[58:59]
	global_load_dwordx4 v[214:217], v186, s[52:53]
	global_load_dwordx4 v[224:227], v186, s[60:61]
	global_load_dwordx4 v[228:231], v186, s[58:59]
	global_load_dwordx4 v[232:235], v187, s[52:53]
	global_load_dwordx4 v[236:239], v187, s[60:61]
	global_load_dwordx4 v[240:243], v187, s[58:59]
	global_load_dwordx4 v[244:247], v190, s[52:53]
	global_load_dwordx4 v[248:251], v190, s[60:61]
	v_pk_fma_f32 v[40:41], v[72:73], v[72:73], v[2:3] op_sel_hi:[1,1,0]
	v_and_b32_e32 v76, 0xffff0000, v38
	v_mul_f32_e32 v2, v71, v71
	v_lshlrev_b32_e32 v75, 16, v39
	v_lshlrev_b32_e32 v74, 16, v38
	v_pk_mul_f32 v[38:39], v[76:77], v[76:77]
	v_lshlrev_b32_e32 v62, 16, v36
	v_and_b32_e32 v63, 0xffff0000, v36
	v_lshlrev_b32_e32 v64, 16, v37
	v_and_b32_e32 v65, 0xffff0000, v37
	v_pk_fma_f32 v[36:37], v[70:71], v[70:71], v[2:3] op_sel_hi:[1,1,0]
	v_pk_fma_f32 v[38:39], v[74:75], v[74:75], v[38:39]
	v_mov_b32_e32 v54, v36
	v_mul_f32_e32 v4, v53, v53
	v_pk_add_f32 v[36:37], v[36:37], v[40:41]
	v_pk_add_f32 v[38:39], v[38:39], v[38:39] op_sel:[0,1] op_sel_hi:[1,0]
	v_mul_f32_e32 v2, v63, v63
	v_mov_b32_e32 v39, v4
	v_lshlrev_b32_e32 v56, 16, v7
	v_and_b32_e32 v57, 0xffff0000, v7
	v_mul_f32_e32 v6, v56, v56
	v_mul_f32_e32 v18, v57, v57
	s_waitcnt vmcnt(26)
	v_and_b32_e32 v69, 0xffff0000, v35
	v_and_b32_e32 v68, 0xffff0000, v34
	v_lshlrev_b32_e32 v67, 16, v35
	v_lshlrev_b32_e32 v66, 16, v34
	v_pk_mul_f32 v[34:35], v[68:69], v[68:69]
	s_waitcnt vmcnt(25)
	v_and_b32_e32 v87, 0xffff0000, v33
	v_pk_fma_f32 v[34:35], v[66:67], v[66:67], v[34:35]
	v_and_b32_e32 v86, 0xffff0000, v32
	s_waitcnt vmcnt(23)
	v_lshlrev_b32_e32 v7, 16, v50
	v_pk_add_f32 v[34:35], v[34:35], v[34:35] op_sel:[0,1] op_sel_hi:[1,0]
	v_lshlrev_b32_e32 v61, 16, v33
	v_lshlrev_b32_e32 v60, 16, v32
	v_pk_mul_f32 v[32:33], v[86:87], v[86:87]
	v_lshlrev_b32_e32 v82, 16, v30
	v_and_b32_e32 v83, 0xffff0000, v30
	v_lshlrev_b32_e32 v84, 16, v31
	v_and_b32_e32 v85, 0xffff0000, v31
	v_and_b32_e32 v5, 0xffff0000, v50
	v_pk_fma_f32 v[32:33], v[60:61], v[60:61], v[32:33]
	v_lshlrev_b32_e32 v50, 16, v51
	v_pk_add_f32 v[32:33], v[32:33], v[32:33] op_sel:[0,1] op_sel_hi:[1,0]
	v_and_b32_e32 v51, 0xffff0000, v51
	v_mul_f32_e32 v4, v50, v50
	v_mov_b32_e32 v52, v55
	s_waitcnt vmcnt(21)
	v_mov_b32_e32 v42, v118
	v_mov_b32_e32 v43, v119
	v_mov_b32_e32 v44, v120
	v_mov_b32_e32 v45, v121
	v_mov_b32_e32 v46, v122
	v_mov_b32_e32 v47, v123
	v_mov_b32_e32 v48, v124
	v_mov_b32_e32 v49, v125
	global_load_dwordx4 v[118:121], v190, s[58:59]
	global_load_dwordx4 v[122:125], v181, s[52:53]
	v_pk_add_f32 v[212:213], v[46:47], 1.0 op_sel_hi:[1,0]
	v_mov_b32_e32 v46, v40
	v_mov_b32_e32 v47, v55
	v_pk_mul_f32 v[40:41], v[54:55], v[46:47]
	v_pk_add_f32 v[48:49], v[48:49], 1.0 op_sel_hi:[1,0]
	v_mov_b32_e32 v37, v41
	v_pk_add_f32 v[36:37], v[36:37], v[38:39]
	v_pk_fma_f32 v[38:39], v[62:63], v[62:63], v[2:3] op_sel_hi:[1,1,0]
	v_mul_f32_e32 v2, v65, v65
	v_pk_fma_f32 v[40:41], v[64:65], v[64:65], v[2:3] op_sel_hi:[1,1,0]
	v_mov_b32_e32 v39, v6
	v_mov_b32_e32 v41, v18
	v_pk_add_f32 v[38:39], v[38:39], v[40:41]
	v_mul_f32_e32 v2, v5, v5
	v_pk_add_f32 v[36:37], v[36:37], v[38:39]
	v_mov_b32_e32 v33, v2
	v_pk_add_f32 v[30:31], v[36:37], v[36:37] op_sel:[0,1] op_sel_hi:[1,0]
	v_mov_b32_e32 v36, v34
	v_mov_b32_e32 v6, v30
	v_mov_b32_e32 v37, v7
	v_pk_add_f32 v[30:31], v[30:31], v[34:35]
	v_pk_mul_f32 v[34:35], v[6:7], v[36:37]
	v_mul_f32_e32 v2, v83, v83
	v_mov_b32_e32 v31, v35
	v_pk_add_f32 v[30:31], v[30:31], v[32:33]
	v_pk_fma_f32 v[32:33], v[82:83], v[82:83], v[2:3] op_sel_hi:[1,1,0]
	v_mul_f32_e32 v2, v85, v85
	v_mul_f32_e32 v18, v51, v51
	v_pk_fma_f32 v[34:35], v[84:85], v[84:85], v[2:3] op_sel_hi:[1,1,0]
	v_mov_b32_e32 v33, v4
	v_mov_b32_e32 v35, v18
	v_pk_add_f32 v[32:33], v[32:33], v[34:35]
	v_mov_b32_e32 v40, v95
	v_pk_add_f32 v[30:31], v[30:31], v[32:33]
	v_mov_b32_e32 v33, v108
	v_mov_b32_e32 v32, v30
	v_mov_b32_e32 v108, v31
	v_pk_add_f32 v[30:31], v[32:33], v[108:109]
	v_mov_b32_e32 v41, v99
	v_mov_b32_e32 v95, v98
	v_mov_b32_dpp v33, v31 quad_perm:[1,0,3,2] row_mask:0xf bank_mask:0xf bound_ctrl:1
	v_mov_b32_dpp v32, v30 quad_perm:[1,0,3,2] row_mask:0xf bank_mask:0xf bound_ctrl:1
	v_pk_add_f32 v[30:31], v[30:31], v[32:33]
	v_mov_b32_e32 v18, v21
	s_nop 0
	v_mov_b32_dpp v33, v31 quad_perm:[2,3,0,1] row_mask:0xf bank_mask:0xf bound_ctrl:1
	v_mov_b32_dpp v32, v30 quad_perm:[2,3,0,1] row_mask:0xf bank_mask:0xf bound_ctrl:1
	v_pk_add_f32 v[30:31], v[30:31], v[32:33]
	s_nop 1
	v_mov_b32_dpp v33, v31 row_half_mirror row_mask:0xf bank_mask:0xf bound_ctrl:1
	v_mov_b32_dpp v32, v30 row_half_mirror row_mask:0xf bank_mask:0xf bound_ctrl:1
	v_pk_add_f32 v[30:31], v[30:31], v[32:33]
	s_nop 1
	v_mov_b32_dpp v33, v31 row_mirror row_mask:0xf bank_mask:0xf bound_ctrl:1
	v_mov_b32_dpp v32, v30 row_mirror row_mask:0xf bank_mask:0xf bound_ctrl:1
	v_pk_add_f32 v[30:31], v[30:31], v[32:33]
	ds_bpermute_b32 v33, v111, v31
	ds_bpermute_b32 v32, v111, v30
	s_waitcnt lgkmcnt(0)
	v_pk_add_f32 v[30:31], v[30:31], v[32:33]
	ds_bpermute_b32 v33, v112, v31
	ds_bpermute_b32 v32, v112, v30
	s_waitcnt lgkmcnt(0)
	v_pk_add_f32 v[30:31], v[30:31], v[32:33]
	s_nop 0
	v_pk_fma_f32 v[108:109], v[30:31], s[0:1], v[188:189] op_sel_hi:[1,0,0]
	s_nop 0
	v_mul_f32_e32 v2, 0x4b800000, v109
	v_cmp_gt_f32_e64 s[0:1], s11, v109
	v_cmp_gt_f32_e32 vcc, s11, v108
	s_nop 0
	v_cndmask_b32_e64 v2, v109, v2, s[0:1]
	v_rsq_f32_e32 v2, v2
	s_nop 0
	v_mul_f32_e32 v4, 0x45800000, v2
	v_cndmask_b32_e64 v2, v2, v4, s[0:1]
	v_pk_mul_f32 v[30:31], v[2:3], v[102:103] op_sel_hi:[0,1]
	v_pk_mul_f32 v[32:33], v[2:3], v[100:101] op_sel_hi:[0,1]
	v_pk_mul_f32 v[32:33], v[42:43], v[32:33]
	v_pk_mul_f32 v[30:31], v[44:45], v[30:31]
	s_mov_b32 s0, 0x40200000
	s_waitcnt vmcnt(22)
	v_mov_b32_e32 v192, v126
	v_mov_b32_e32 v193, v127
	v_mov_b32_e32 v194, v128
	v_mov_b32_e32 v195, v129
	global_load_dwordx4 v[126:129], v181, s[56:57]
	v_pk_fma_f32 v[46:47], v[48:49], v[30:31], v[194:195]
	v_pk_fma_f32 v[48:49], v[212:213], v[32:33], v[192:193]
	v_add_co_u32_e64 v100, s[0:1], s0, v28
	v_cvt_pk_bf16_f32 v30, v48, v49
	v_cvt_pk_bf16_f32 v31, v46, v47
	v_addc_co_u32_e64 v101, s[0:1], 0, v29, s[0:1]
	global_store_dwordx2 v[100:101], v[30:31], off
	s_nop 0
	v_pk_mul_f32 v[40:41], v[2:3], v[40:41] op_sel_hi:[0,1]
	v_pk_mul_f32 v[42:43], v[2:3], v[94:95] op_sel_hi:[0,1]
	v_pk_mul_f32 v[90:91], v[2:3], v[90:91] op_sel_hi:[0,1]
	v_pk_mul_f32 v[26:27], v[2:3], v[26:27] op_sel_hi:[0,1]
	v_pk_mul_f32 v[22:23], v[2:3], v[22:23] op_sel_hi:[0,1]
	v_pk_mul_f32 v[80:81], v[2:3], v[80:81] op_sel_hi:[0,1]
	v_pk_mul_f32 v[78:79], v[2:3], v[78:79] op_sel_hi:[0,1]
	v_pk_mul_f32 v[58:59], v[2:3], v[58:59] op_sel_hi:[0,1]
	v_pk_mul_f32 v[18:19], v[2:3], v[18:19] op_sel_hi:[0,1]
	s_waitcnt vmcnt(23)
	v_mov_b32_e32 v28, v130
	v_mov_b32_e32 v29, v131
	v_mov_b32_e32 v30, v132
	v_mov_b32_e32 v31, v133
	global_load_dwordx4 v[130:133], v181, s[54:55]
	v_pk_mul_f32 v[28:29], v[28:29], v[42:43]
	v_pk_mul_f32 v[30:31], v[30:31], v[40:41]
	s_waitcnt vmcnt(23)
	v_mov_b32_e32 v32, v134
	v_mov_b32_e32 v33, v135
	v_mov_b32_e32 v34, v136
	v_mov_b32_e32 v35, v137
	global_load_dwordx4 v[134:137], v181, s[52:53] offset:1024
	v_pk_add_f32 v[34:35], v[34:35], 1.0 op_sel_hi:[1,0]
	v_pk_add_f32 v[32:33], v[32:33], 1.0 op_sel_hi:[1,0]
	s_waitcnt vmcnt(23)
	v_mov_b32_e32 v36, v138
	v_mov_b32_e32 v37, v139
	v_mov_b32_e32 v38, v140
	v_mov_b32_e32 v39, v141
	global_load_dwordx4 v[138:141], v182, s[56:57]
	v_pk_fma_f32 v[42:43], v[34:35], v[30:31], v[38:39]
	v_pk_fma_f32 v[44:45], v[32:33], v[28:29], v[36:37]
	v_cvt_pk_bf16_f32 v29, v42, v43
	v_cvt_pk_bf16_f32 v28, v44, v45
	global_store_dwordx2 v[100:101], v[28:29], off offset:512
	s_nop 0
	v_pk_mul_f32 v[40:41], v[2:3], v[96:97] op_sel_hi:[0,1]
	s_waitcnt vmcnt(24)
	v_mov_b32_e32 v28, v142
	v_mov_b32_e32 v29, v143
	v_mov_b32_e32 v30, v144
	v_mov_b32_e32 v31, v145
	global_load_dwordx4 v[142:145], v182, s[54:55]
	v_pk_mul_f32 v[28:29], v[28:29], v[90:91]
	v_pk_mul_f32 v[30:31], v[30:31], v[40:41]
	s_waitcnt vmcnt(24)
	v_mov_b32_e32 v32, v146
	v_mov_b32_e32 v33, v147
	v_mov_b32_e32 v34, v148
	v_mov_b32_e32 v35, v149
	global_load_dwordx4 v[146:149], v181, s[52:53] offset:2048
	v_pk_add_f32 v[34:35], v[34:35], 1.0 op_sel_hi:[1,0]
	v_pk_add_f32 v[32:33], v[32:33], 1.0 op_sel_hi:[1,0]
	s_waitcnt vmcnt(24)
	v_mov_b32_e32 v36, v150
	v_mov_b32_e32 v37, v151
	v_mov_b32_e32 v38, v152
	v_mov_b32_e32 v39, v153
	global_load_dwordx4 v[150:153], v183, s[56:57]
	v_pk_fma_f32 v[38:39], v[34:35], v[30:31], v[38:39]
	v_pk_fma_f32 v[40:41], v[32:33], v[28:29], v[36:37]
	v_cvt_pk_bf16_f32 v29, v38, v39
	v_cvt_pk_bf16_f32 v28, v40, v41
	global_store_dwordx2 v[100:101], v[28:29], off offset:1024
	s_nop 0
	v_mov_b32_e32 v90, v89
	v_mov_b32_e32 v91, v93
	v_mov_b32_e32 v89, v92
	v_pk_mul_f32 v[90:91], v[2:3], v[90:91] op_sel_hi:[0,1]
	v_pk_mul_f32 v[88:89], v[2:3], v[88:89] op_sel_hi:[0,1]
	s_waitcnt vmcnt(25)
	v_mov_b32_e32 v28, v154
	v_mov_b32_e32 v29, v155
	v_mov_b32_e32 v30, v156
	v_mov_b32_e32 v31, v157
	global_load_dwordx4 v[154:157], v183, s[54:55]
	v_pk_mul_f32 v[22:23], v[22:23], v[28:29]
	v_pk_mul_f32 v[24:25], v[26:27], v[30:31]
	s_waitcnt vmcnt(25)
	v_mov_b32_e32 v32, v158
	v_mov_b32_e32 v33, v159
	v_mov_b32_e32 v34, v160
	v_mov_b32_e32 v35, v161
	global_load_dwordx4 v[158:161], v181, s[52:53] offset:3072
	v_pk_add_f32 v[26:27], v[34:35], 1.0 op_sel_hi:[1,0]
	v_pk_add_f32 v[28:29], v[32:33], 1.0 op_sel_hi:[1,0]
	s_waitcnt vmcnt(25)
	v_mov_b32_e32 v94, v162
	v_mov_b32_e32 v95, v163
	v_mov_b32_e32 v96, v164
	v_mov_b32_e32 v97, v165
	global_load_dwordx4 v[162:165], v184, s[56:57]
	v_pk_fma_f32 v[30:31], v[24:25], v[26:27], v[96:97]
	v_pk_fma_f32 v[32:33], v[22:23], v[28:29], v[94:95]
	v_cvt_pk_bf16_f32 v23, v30, v31
	v_cvt_pk_bf16_f32 v22, v32, v33
	global_store_dwordx2 v[100:101], v[22:23], off offset:1536
	s_nop 0
	v_mov_b32_e32 v34, v105
	v_mov_b32_e32 v35, v107
	v_mov_b32_e32 v105, v106
	v_pk_mul_f32 v[34:35], v[2:3], v[34:35] op_sel_hi:[0,1]
	v_pk_mul_f32 v[36:37], v[2:3], v[104:105] op_sel_hi:[0,1]
	v_mul_f32_e32 v2, 0x4b800000, v108
	v_cndmask_b32_e32 v2, v108, v2, vcc
	v_rsq_f32_e32 v2, v2
	s_waitcnt vmcnt(26)
	v_mov_b32_e32 v22, v166
	v_mov_b32_e32 v23, v167
	v_mov_b32_e32 v24, v168
	v_mov_b32_e32 v25, v169
	global_load_dwordx4 v[166:169], v184, s[54:55]
	v_pk_mul_f32 v[22:23], v[36:37], v[22:23]
	v_pk_mul_f32 v[24:25], v[34:35], v[24:25]
	s_waitcnt vmcnt(26)
	v_mov_b32_e32 v26, v170
	v_mov_b32_e32 v27, v171
	v_mov_b32_e32 v28, v172
	v_mov_b32_e32 v29, v173
	global_load_dwordx4 v[170:173], v185, s[52:53]
	v_pk_add_f32 v[28:29], v[28:29], 1.0 op_sel_hi:[1,0]
	v_pk_add_f32 v[26:27], v[26:27], 1.0 op_sel_hi:[1,0]
	s_waitcnt vmcnt(26)
	v_mov_b32_e32 v94, v174
	v_mov_b32_e32 v95, v175
	v_mov_b32_e32 v96, v176
	v_mov_b32_e32 v97, v177
	global_load_dwordx4 v[174:177], v185, s[56:57]
	v_pk_fma_f32 v[34:35], v[24:25], v[28:29], v[96:97]
	v_pk_fma_f32 v[36:37], v[22:23], v[26:27], v[94:95]
	v_cvt_pk_bf16_f32 v23, v34, v35
	v_cvt_pk_bf16_f32 v22, v36, v37
	global_store_dwordx2 v[100:101], v[22:23], off offset:2048
	s_nop 0
	v_mul_f32_e32 v4, 0x45800000, v2
	v_cndmask_b32_e32 v2, v2, v4, vcc
	v_pk_mul_f32 v[70:71], v[2:3], v[70:71] op_sel_hi:[0,1]
	v_pk_mul_f32 v[62:63], v[2:3], v[62:63] op_sel_hi:[0,1]
	v_pk_mul_f32 v[56:57], v[2:3], v[56:57] op_sel_hi:[0,1]
	v_pk_mul_f32 v[52:53], v[2:3], v[52:53] op_sel_hi:[0,1]
	v_pk_mul_f32 v[82:83], v[2:3], v[82:83] op_sel_hi:[0,1]
	v_mov_b32_e32 v4, v7
	v_pk_mul_f32 v[50:51], v[2:3], v[50:51] op_sel_hi:[0,1]
	v_pk_mul_f32 v[4:5], v[2:3], v[4:5] op_sel_hi:[0,1]
	s_waitcnt vmcnt(27)
	v_mov_b32_e32 v22, v214
	v_mov_b32_e32 v23, v215
	v_mov_b32_e32 v24, v216
	v_mov_b32_e32 v25, v217
	global_load_dwordx4 v[214:217], v185, s[54:55]
	v_pk_mul_f32 v[22:23], v[88:89], v[22:23]
	v_pk_mul_f32 v[24:25], v[90:91], v[24:25]
	s_waitcnt vmcnt(27)
	v_mov_b32_e32 v26, v224
	v_mov_b32_e32 v27, v225
	v_mov_b32_e32 v28, v226
	v_mov_b32_e32 v29, v227
	global_load_dwordx4 v[224:227], v186, s[52:53]
	v_pk_add_f32 v[28:29], v[28:29], 1.0 op_sel_hi:[1,0]
	v_pk_add_f32 v[88:89], v[26:27], 1.0 op_sel_hi:[1,0]
	s_waitcnt vmcnt(27)
	v_mov_b32_e32 v94, v228
	v_mov_b32_e32 v95, v229
	v_mov_b32_e32 v96, v230
	v_mov_b32_e32 v97, v231
	global_load_dwordx4 v[228:231], v186, s[56:57]
	v_pk_fma_f32 v[26:27], v[24:25], v[28:29], v[96:97]
	v_pk_fma_f32 v[28:29], v[22:23], v[88:89], v[94:95]
	v_cvt_pk_bf16_f32 v23, v26, v27
	v_cvt_pk_bf16_f32 v22, v28, v29
	global_store_dwordx2 v[100:101], v[22:23], off offset:2560
	s_nop 0
	v_lshl_add_u64 v[96:97], v[12:13], 0, s[50:51]
	s_waitcnt vmcnt(28)
	v_mov_b32_e32 v22, v232
	v_mov_b32_e32 v23, v233
	v_mov_b32_e32 v24, v234
	v_mov_b32_e32 v25, v235
	global_load_dwordx4 v[232:235], v186, s[54:55]
	v_pk_mul_f32 v[78:79], v[78:79], v[22:23]
	v_pk_mul_f32 v[22:23], v[80:81], v[24:25]
	s_waitcnt vmcnt(28)
	v_mov_b32_e32 v88, v236
	v_mov_b32_e32 v89, v237
	v_mov_b32_e32 v90, v238
	v_mov_b32_e32 v91, v239
	global_load_dwordx4 v[236:239], v187, s[52:53]
	v_pk_add_f32 v[24:25], v[90:91], 1.0 op_sel_hi:[1,0]
	v_pk_add_f32 v[80:81], v[88:89], 1.0 op_sel_hi:[1,0]
	s_waitcnt vmcnt(28)
	v_mov_b32_e32 v92, v240
	v_mov_b32_e32 v93, v241
	v_mov_b32_e32 v94, v242
	v_mov_b32_e32 v95, v243
	global_load_dwordx4 v[240:243], v187, s[56:57]
	v_pk_fma_f32 v[22:23], v[22:23], v[24:25], v[94:95]
	v_pk_fma_f32 v[24:25], v[78:79], v[80:81], v[92:93]
	v_cvt_pk_bf16_f32 v79, v22, v23
	v_cvt_pk_bf16_f32 v78, v24, v25
	global_store_dwordx2 v[100:101], v[78:79], off offset:3072
	s_nop 0
	s_waitcnt vmcnt(29)
	v_mov_b32_e32 v78, v244
	v_mov_b32_e32 v79, v245
	v_mov_b32_e32 v80, v246
	v_mov_b32_e32 v81, v247
	global_load_dwordx4 v[244:247], v187, s[54:55]
	v_pk_mul_f32 v[20:21], v[18:19], v[78:79]
	v_pk_mul_f32 v[18:19], v[58:59], v[80:81]
	s_waitcnt vmcnt(29)
	v_mov_b32_e32 v88, v248
	v_mov_b32_e32 v89, v249
	v_mov_b32_e32 v90, v250
	v_mov_b32_e32 v91, v251
	global_load_dwordx4 v[248:251], v190, s[52:53]
	v_pk_add_f32 v[58:59], v[90:91], 1.0 op_sel_hi:[1,0]
	v_pk_add_f32 v[78:79], v[88:89], 1.0 op_sel_hi:[1,0]
	s_waitcnt vmcnt(29)
	v_mov_b32_e32 v92, v118
	v_mov_b32_e32 v93, v119
	v_mov_b32_e32 v94, v120
	v_mov_b32_e32 v95, v121
	global_load_dwordx4 v[118:121], v190, s[56:57]
	v_pk_fma_f32 v[18:19], v[18:19], v[58:59], v[94:95]
	v_pk_fma_f32 v[20:21], v[20:21], v[78:79], v[92:93]
	v_cvt_pk_bf16_f32 v59, v18, v19
	v_cvt_pk_bf16_f32 v58, v20, v21
	global_store_dwordx2 v[100:101], v[58:59], off offset:3584
	v_pk_mul_f32 v[58:59], v[2:3], v[72:73] op_sel_hi:[0,1]
	s_waitcnt vmcnt(30)
	v_mov_b32_e32 v78, v122
	v_mov_b32_e32 v79, v123
	v_mov_b32_e32 v80, v124
	v_mov_b32_e32 v81, v125
	global_load_dwordx4 v[122:125], v190, s[54:55]
	v_pk_mul_f32 v[72:73], v[78:79], v[70:71]
	v_pk_mul_f32 v[58:59], v[80:81], v[58:59]
	s_waitcnt vmcnt(30)
	v_mov_b32_e32 v88, v126
	v_mov_b32_e32 v89, v127
	v_mov_b32_e32 v90, v128
	v_mov_b32_e32 v91, v129
	v_pk_add_f32 v[70:71], v[90:91], 1.0 op_sel_hi:[1,0]
	v_pk_add_f32 v[78:79], v[88:89], 1.0 op_sel_hi:[1,0]
	s_waitcnt vmcnt(28)
	v_mov_b32_e32 v92, v130
	v_mov_b32_e32 v93, v131
	v_mov_b32_e32 v94, v132
	v_mov_b32_e32 v95, v133
	v_pk_fma_f32 v[70:71], v[70:71], v[58:59], v[94:95]
	v_pk_fma_f32 v[72:73], v[78:79], v[72:73], v[92:93]
	v_cvt_pk_bf16_f32 v59, v70, v71
	v_cvt_pk_bf16_f32 v58, v72, v73
	global_store_dwordx2 v[96:97], v[58:59], off
	v_mov_b32_e32 v58, v75
	v_mov_b32_e32 v59, v77
	v_mov_b32_e32 v75, v76
	v_pk_mul_f32 v[58:59], v[2:3], v[58:59] op_sel_hi:[0,1]
	v_pk_mul_f32 v[74:75], v[2:3], v[74:75] op_sel_hi:[0,1]
	s_waitcnt vmcnt(28)
	v_mov_b32_e32 v78, v134
	v_mov_b32_e32 v79, v135
	v_mov_b32_e32 v80, v136
	v_mov_b32_e32 v81, v137
	v_pk_mul_f32 v[74:75], v[78:79], v[74:75]
	v_pk_mul_f32 v[58:59], v[80:81], v[58:59]
	s_waitcnt vmcnt(27)
	v_mov_b32_e32 v88, v138
	v_mov_b32_e32 v89, v139
	v_mov_b32_e32 v90, v140
	v_mov_b32_e32 v91, v141
	v_pk_add_f32 v[76:77], v[90:91], 1.0 op_sel_hi:[1,0]
	v_pk_add_f32 v[80:81], v[88:89], 1.0 op_sel_hi:[1,0]
	s_waitcnt vmcnt(25)
	v_mov_b32_e32 v92, v142
	v_mov_b32_e32 v93, v143
	v_mov_b32_e32 v94, v144
	v_mov_b32_e32 v95, v145
	v_pk_fma_f32 v[78:79], v[76:77], v[58:59], v[94:95]
	v_pk_fma_f32 v[80:81], v[80:81], v[74:75], v[92:93]
	v_cvt_pk_bf16_f32 v59, v78, v79
	v_cvt_pk_bf16_f32 v58, v80, v81
	global_store_dwordx2 v[96:97], v[58:59], off offset:512
	v_pk_mul_f32 v[58:59], v[2:3], v[64:65] op_sel_hi:[0,1]
	s_waitcnt vmcnt(25)
	v_mov_b32_e32 v74, v146
	v_mov_b32_e32 v75, v147
	v_mov_b32_e32 v76, v148
	v_mov_b32_e32 v77, v149
	v_pk_mul_f32 v[62:63], v[74:75], v[62:63]
	v_pk_mul_f32 v[58:59], v[76:77], v[58:59]
	s_waitcnt vmcnt(24)
	v_mov_b32_e32 v88, v150
	v_mov_b32_e32 v89, v151
	v_mov_b32_e32 v90, v152
	v_mov_b32_e32 v91, v153
	v_pk_add_f32 v[64:65], v[90:91], 1.0 op_sel_hi:[1,0]
	v_pk_add_f32 v[76:77], v[88:89], 1.0 op_sel_hi:[1,0]
	s_waitcnt vmcnt(22)
	v_mov_b32_e32 v92, v154
	v_mov_b32_e32 v93, v155
	v_mov_b32_e32 v94, v156
	v_mov_b32_e32 v95, v157
	v_pk_fma_f32 v[74:75], v[64:65], v[58:59], v[94:95]
	v_pk_fma_f32 v[76:77], v[76:77], v[62:63], v[92:93]
	v_cvt_pk_bf16_f32 v59, v74, v75
	v_cvt_pk_bf16_f32 v58, v76, v77
	global_store_dwordx2 v[96:97], v[58:59], off offset:1024
	s_waitcnt vmcnt(22)
	v_mov_b32_e32 v62, v158
	v_mov_b32_e32 v63, v159
	v_mov_b32_e32 v64, v160
	v_mov_b32_e32 v65, v161
	v_pk_mul_f32 v[52:53], v[52:53], v[62:63]
	v_pk_mul_f32 v[54:55], v[56:57], v[64:65]
	s_waitcnt vmcnt(21)
	v_mov_b32_e32 v88, v162
	v_mov_b32_e32 v89, v163
	v_mov_b32_e32 v90, v164
	v_mov_b32_e32 v91, v165
	v_pk_add_f32 v[56:57], v[90:91], 1.0 op_sel_hi:[1,0]
	v_pk_add_f32 v[58:59], v[88:89], 1.0 op_sel_hi:[1,0]
	s_waitcnt vmcnt(19)
	v_mov_b32_e32 v92, v166
	v_mov_b32_e32 v93, v167
	v_mov_b32_e32 v94, v168
	v_mov_b32_e32 v95, v169
	v_pk_fma_f32 v[62:63], v[54:55], v[56:57], v[94:95]
	v_pk_fma_f32 v[64:65], v[52:53], v[58:59], v[92:93]
	v_cvt_pk_bf16_f32 v53, v62, v63
	v_cvt_pk_bf16_f32 v52, v64, v65
	global_store_dwordx2 v[96:97], v[52:53], off offset:1536
	s_nop 0
	v_mov_b32_e32 v92, v67
	v_mov_b32_e32 v93, v69
	v_mov_b32_e32 v67, v68
	v_pk_mul_f32 v[92:93], v[2:3], v[92:93] op_sel_hi:[0,1]
	v_pk_mul_f32 v[66:67], v[2:3], v[66:67] op_sel_hi:[0,1]
	s_waitcnt vmcnt(19)
	v_mov_b32_e32 v52, v170
	v_mov_b32_e32 v53, v171
	v_mov_b32_e32 v54, v172
	v_mov_b32_e32 v55, v173
	v_pk_mul_f32 v[52:53], v[66:67], v[52:53]
	v_pk_mul_f32 v[54:55], v[92:93], v[54:55]
	s_waitcnt vmcnt(18)
	v_mov_b32_e32 v56, v174
	v_mov_b32_e32 v57, v175
	v_mov_b32_e32 v58, v176
	v_mov_b32_e32 v59, v177
	v_pk_add_f32 v[58:59], v[58:59], 1.0 op_sel_hi:[1,0]
	v_pk_add_f32 v[56:57], v[56:57], 1.0 op_sel_hi:[1,0]
	s_waitcnt vmcnt(16)
	v_mov_b32_e32 v88, v214
	v_mov_b32_e32 v89, v215
	v_mov_b32_e32 v90, v216
	v_mov_b32_e32 v91, v217
	v_pk_fma_f32 v[66:67], v[54:55], v[58:59], v[90:91]
	v_pk_fma_f32 v[68:69], v[52:53], v[56:57], v[88:89]
	v_cvt_pk_bf16_f32 v53, v66, v67
	v_cvt_pk_bf16_f32 v52, v68, v69
	global_store_dwordx2 v[96:97], v[52:53], off offset:2048
	s_nop 0
	v_mov_b32_e32 v92, v61
	v_mov_b32_e32 v93, v87
	v_mov_b32_e32 v61, v86
	v_pk_mul_f32 v[92:93], v[2:3], v[92:93] op_sel_hi:[0,1]
	v_pk_mul_f32 v[60:61], v[2:3], v[60:61] op_sel_hi:[0,1]
	s_waitcnt vmcnt(16)
	v_mov_b32_e32 v52, v224
	v_mov_b32_e32 v53, v225
	v_mov_b32_e32 v54, v226
	v_mov_b32_e32 v55, v227
	v_pk_mul_f32 v[52:53], v[60:61], v[52:53]
	v_pk_mul_f32 v[54:55], v[92:93], v[54:55]
	s_waitcnt vmcnt(15)
	v_mov_b32_e32 v56, v228
	v_mov_b32_e32 v57, v229
	v_mov_b32_e32 v58, v230
	v_mov_b32_e32 v59, v231
	v_pk_add_f32 v[58:59], v[58:59], 1.0 op_sel_hi:[1,0]
	v_pk_add_f32 v[56:57], v[56:57], 1.0 op_sel_hi:[1,0]
	s_waitcnt vmcnt(13)
	v_mov_b32_e32 v88, v232
	v_mov_b32_e32 v89, v233
	v_mov_b32_e32 v90, v234
	v_mov_b32_e32 v91, v235
	v_pk_fma_f32 v[58:59], v[54:55], v[58:59], v[90:91]
	v_pk_fma_f32 v[60:61], v[52:53], v[56:57], v[88:89]
	v_cvt_pk_bf16_f32 v53, v58, v59
	v_cvt_pk_bf16_f32 v52, v60, v61
	global_store_dwordx2 v[96:97], v[52:53], off offset:2560
	s_nop 0
	v_pk_mul_f32 v[56:57], v[2:3], v[84:85] op_sel_hi:[0,1]
	s_waitcnt vmcnt(13)
	v_mov_b32_e32 v52, v236
	v_mov_b32_e32 v53, v237
	v_mov_b32_e32 v54, v238
	v_mov_b32_e32 v55, v239
	v_pk_mul_f32 v[52:53], v[82:83], v[52:53]
	v_pk_mul_f32 v[54:55], v[56:57], v[54:55]
	s_waitcnt vmcnt(12)
	v_mov_b32_e32 v86, v240
	v_mov_b32_e32 v87, v241
	v_mov_b32_e32 v88, v242
	v_mov_b32_e32 v89, v243
	v_pk_add_f32 v[56:57], v[88:89], 1.0 op_sel_hi:[1,0]
	v_pk_add_f32 v[82:83], v[86:87], 1.0 op_sel_hi:[1,0]
	s_waitcnt vmcnt(10)
	v_mov_b32_e32 v90, v244
	v_mov_b32_e32 v91, v245
	v_mov_b32_e32 v92, v246
	v_mov_b32_e32 v93, v247
	v_pk_fma_f32 v[54:55], v[54:55], v[56:57], v[92:93]
	v_pk_fma_f32 v[56:57], v[52:53], v[82:83], v[90:91]
	v_cvt_pk_bf16_f32 v53, v54, v55
	v_cvt_pk_bf16_f32 v52, v56, v57
	global_store_dwordx2 v[96:97], v[52:53], off offset:3072
	s_waitcnt vmcnt(10)
	v_mov_b32_e32 v82, v248
	v_mov_b32_e32 v83, v249
	v_mov_b32_e32 v84, v250
	v_mov_b32_e32 v85, v251
	v_pk_mul_f32 v[4:5], v[4:5], v[82:83]
	v_pk_mul_f32 v[6:7], v[50:51], v[84:85]
	s_waitcnt vmcnt(9)
	v_mov_b32_e32 v86, v118
	v_mov_b32_e32 v87, v119
	v_mov_b32_e32 v88, v120
	v_mov_b32_e32 v89, v121
	v_pk_add_f32 v[50:51], v[88:89], 1.0 op_sel_hi:[1,0]
	v_pk_add_f32 v[52:53], v[86:87], 1.0 op_sel_hi:[1,0]
	s_waitcnt vmcnt(7)
	v_mov_b32_e32 v90, v122
	v_mov_b32_e32 v91, v123
	v_mov_b32_e32 v92, v124
	v_mov_b32_e32 v93, v125
	v_pk_fma_f32 v[50:51], v[6:7], v[50:51], v[92:93]
	v_pk_fma_f32 v[52:53], v[4:5], v[52:53], v[90:91]
	v_cvt_pk_bf16_f32 v5, v50, v51
	v_cvt_pk_bf16_f32 v4, v52, v53
	global_store_dwordx2 v[96:97], v[4:5], off offset:3584
	v_add_u32_e32 v118, 0x10400, v110
	v_add_u32_e32 v119, 0x10800, v110
	v_add_u32_e32 v120, 0x10c00, v110
	v_add_u32_e32 v121, 0x11000, v110
	v_add_u32_e32 v122, 0x11400, v110
	v_add_u32_e32 v123, 0x11800, v110
	v_add_u32_e32 v124, 0x11c00, v110
	v_add_u32_e32 v125, 0x12000, v110
	v_add_u32_e32 v126, 0x12400, v110
	v_add_u32_e32 v127, 0x12800, v110
	v_add_u32_e32 v128, 0x12c00, v110
	v_add_u32_e32 v129, 0x13000, v110
	v_add_u32_e32 v130, 0x13400, v110
	v_add_u32_e32 v131, 0x13800, v110
	v_add_u32_e32 v132, 0x13c00, v110
	v_add_u32_e32 v133, 0x14000, v110
	v_add_u32_e32 v134, 0x14400, v110
	v_add_u32_e32 v135, 0x14800, v110
	v_add_u32_e32 v136, 0x14c00, v110
	v_add_u32_e32 v137, 0x15000, v110
	v_add_u32_e32 v138, 0x15400, v110
	v_add_u32_e32 v139, 0x15800, v110
	v_add_u32_e32 v140, 0x15c00, v110
	v_add_u32_e32 v141, 0x16000, v110
	v_add_u32_e32 v142, 0x16400, v110
	v_add_u32_e32 v143, 0x16800, v110
	v_add_u32_e32 v144, 0x16c00, v110
	v_add_u32_e32 v145, 0x17000, v110
	v_add_u32_e32 v146, 0x17400, v110
	v_add_u32_e32 v147, 0x17800, v110
	v_add_u32_e32 v148, 0x17c00, v110
	v_add_u32_e32 v149, 0x18000, v110
	v_add_u32_e32 v150, 0x18400, v110
	v_add_u32_e32 v151, 0x18800, v110
	v_add_u32_e32 v152, 0x18c00, v110
	v_add_u32_e32 v153, 0x19000, v110
	v_add_u32_e32 v154, 0x19400, v110
	v_add_u32_e32 v155, 0x19800, v110
	v_add_u32_e32 v156, 0x19c00, v110
	v_add_u32_e32 v157, 0x1a000, v110
	v_add_u32_e32 v158, 0x1a400, v110
	v_add_u32_e32 v159, 0x1a800, v110
	v_add_u32_e32 v160, 0x1ac00, v110
	v_add_u32_e32 v161, 0x1b000, v110
	v_add_u32_e32 v162, 0x1b400, v110
	v_add_u32_e32 v163, 0x1b800, v110
	v_add_u32_e32 v164, 0x1bc00, v110
	v_add_u32_e32 v165, 0x1c000, v110
	v_add_u32_e32 v166, 0x1c400, v110
	v_add_u32_e32 v167, 0x1c800, v110
	v_add_u32_e32 v168, 0x1cc00, v110
	v_add_u32_e32 v169, 0x1d000, v110
	v_add_u32_e32 v170, 0x1d400, v110
	v_add_u32_e32 v171, 0x1d800, v110
	v_add_u32_e32 v172, 0x1dc00, v110
	v_add_u32_e32 v173, 0x1e000, v110
	v_add_u32_e32 v174, 0x1e400, v110
	v_add_u32_e32 v175, 0x1e800, v110
	v_add_u32_e32 v176, 0x1ec00, v110
	v_add_u32_e32 v177, 0x1f000, v110
	ds_read_b128 v[224:227], v110
	ds_read_b128 v[228:231], v110 offset:1024
	ds_read_b128 v[232:235], v110 offset:2048
	ds_read_b128 v[236:239], v110 offset:3072
	ds_read_b128 v[240:243], v110 offset:4096
	ds_read_b128 v[244:247], v110 offset:5120
	s_waitcnt lgkmcnt(5)
	v_pk_mul_f32 v[248:249], v[224:225], v[48:49]
	v_pk_mul_f32 v[250:251], v[224:225], v[72:73]
	v_pk_fma_f32 v[248:249], v[226:227], v[46:47], v[248:249]
	v_pk_fma_f32 v[250:251], v[226:227], v[70:71], v[250:251]
	ds_read_b128 v[224:227], v110 offset:6144
	s_waitcnt lgkmcnt(5)
	v_pk_fma_f32 v[248:249], v[228:229], v[44:45], v[248:249]
	v_pk_fma_f32 v[250:251], v[228:229], v[80:81], v[250:251]
	v_pk_fma_f32 v[248:249], v[230:231], v[42:43], v[248:249]
	v_pk_fma_f32 v[250:251], v[230:231], v[78:79], v[250:251]
	ds_read_b128 v[228:231], v110 offset:7168
	s_waitcnt lgkmcnt(5)
	v_pk_fma_f32 v[248:249], v[232:233], v[40:41], v[248:249]
	v_pk_fma_f32 v[250:251], v[232:233], v[76:77], v[250:251]
	v_pk_fma_f32 v[248:249], v[234:235], v[38:39], v[248:249]
	v_pk_fma_f32 v[250:251], v[234:235], v[74:75], v[250:251]
	ds_read_b128 v[232:235], v110 offset:8192
	s_waitcnt lgkmcnt(5)
	v_pk_fma_f32 v[248:249], v[236:237], v[32:33], v[248:249]
	v_pk_fma_f32 v[250:251], v[236:237], v[64:65], v[250:251]
	v_pk_fma_f32 v[248:249], v[238:239], v[30:31], v[248:249]
	v_pk_fma_f32 v[250:251], v[238:239], v[62:63], v[250:251]
	ds_read_b128 v[236:239], v110 offset:9216
	s_waitcnt lgkmcnt(5)
	v_pk_fma_f32 v[248:249], v[240:241], v[36:37], v[248:249]
	v_pk_fma_f32 v[250:251], v[240:241], v[68:69], v[250:251]
	v_pk_fma_f32 v[248:249], v[242:243], v[34:35], v[248:249]
	v_pk_fma_f32 v[250:251], v[242:243], v[66:67], v[250:251]
	ds_read_b128 v[240:243], v110 offset:10240
	s_waitcnt lgkmcnt(5)
	v_pk_fma_f32 v[248:249], v[244:245], v[28:29], v[248:249]
	v_pk_fma_f32 v[250:251], v[244:245], v[60:61], v[250:251]
	v_pk_fma_f32 v[248:249], v[246:247], v[26:27], v[248:249]
	v_pk_fma_f32 v[250:251], v[246:247], v[58:59], v[250:251]
	ds_read_b128 v[244:247], v110 offset:11264
	s_waitcnt lgkmcnt(5)
	v_pk_fma_f32 v[248:249], v[224:225], v[24:25], v[248:249]
	v_pk_fma_f32 v[250:251], v[224:225], v[56:57], v[250:251]
	v_pk_fma_f32 v[248:249], v[226:227], v[22:23], v[248:249]
	v_pk_fma_f32 v[250:251], v[226:227], v[54:55], v[250:251]
	ds_read_b128 v[224:227], v110 offset:12288
	s_waitcnt lgkmcnt(5)
	v_pk_fma_f32 v[248:249], v[228:229], v[20:21], v[248:249]
	v_pk_fma_f32 v[250:251], v[228:229], v[52:53], v[250:251]
	v_pk_fma_f32 v[248:249], v[230:231], v[18:19], v[248:249]
	v_pk_fma_f32 v[250:251], v[230:231], v[50:51], v[250:251]
	ds_read_b128 v[228:231], v110 offset:13312
	v_add_f32_e32 v2, v248, v249
	v_add_f32_e32 v82, v250, v251
	s_waitcnt lgkmcnt(5)
	v_pk_mul_f32 v[248:249], v[232:233], v[48:49]
	v_pk_mul_f32 v[250:251], v[232:233], v[72:73]
	v_pk_fma_f32 v[248:249], v[234:235], v[46:47], v[248:249]
	v_pk_fma_f32 v[250:251], v[234:235], v[70:71], v[250:251]
	ds_read_b128 v[232:235], v110 offset:14336
	s_waitcnt lgkmcnt(5)
	v_pk_fma_f32 v[248:249], v[236:237], v[44:45], v[248:249]
	v_pk_fma_f32 v[250:251], v[236:237], v[80:81], v[250:251]
	v_pk_fma_f32 v[248:249], v[238:239], v[42:43], v[248:249]
	v_pk_fma_f32 v[250:251], v[238:239], v[78:79], v[250:251]
	ds_read_b128 v[236:239], v110 offset:15360
	s_waitcnt lgkmcnt(5)
	v_pk_fma_f32 v[248:249], v[240:241], v[40:41], v[248:249]
	v_pk_fma_f32 v[250:251], v[240:241], v[76:77], v[250:251]
	v_pk_fma_f32 v[248:249], v[242:243], v[38:39], v[248:249]
	v_pk_fma_f32 v[250:251], v[242:243], v[74:75], v[250:251]
	ds_read_b128 v[240:243], v110 offset:16384
	s_waitcnt lgkmcnt(5)
	v_pk_fma_f32 v[248:249], v[244:245], v[32:33], v[248:249]
	v_pk_fma_f32 v[250:251], v[244:245], v[64:65], v[250:251]
	v_pk_fma_f32 v[248:249], v[246:247], v[30:31], v[248:249]
	v_pk_fma_f32 v[250:251], v[246:247], v[62:63], v[250:251]
	ds_read_b128 v[244:247], v110 offset:17408
	s_waitcnt lgkmcnt(5)
	v_pk_fma_f32 v[248:249], v[224:225], v[36:37], v[248:249]
	v_pk_fma_f32 v[250:251], v[224:225], v[68:69], v[250:251]
	v_pk_fma_f32 v[248:249], v[226:227], v[34:35], v[248:249]
	v_pk_fma_f32 v[250:251], v[226:227], v[66:67], v[250:251]
	ds_read_b128 v[224:227], v110 offset:18432
	s_waitcnt lgkmcnt(5)
	v_pk_fma_f32 v[248:249], v[228:229], v[28:29], v[248:249]
	v_pk_fma_f32 v[250:251], v[228:229], v[60:61], v[250:251]
	v_pk_fma_f32 v[248:249], v[230:231], v[26:27], v[248:249]
	v_pk_fma_f32 v[250:251], v[230:231], v[58:59], v[250:251]
	ds_read_b128 v[228:231], v110 offset:19456
	s_waitcnt lgkmcnt(5)
	v_pk_fma_f32 v[248:249], v[232:233], v[24:25], v[248:249]
	v_pk_fma_f32 v[250:251], v[232:233], v[56:57], v[250:251]
	v_pk_fma_f32 v[248:249], v[234:235], v[22:23], v[248:249]
	v_pk_fma_f32 v[250:251], v[234:235], v[54:55], v[250:251]
	ds_read_b128 v[232:235], v110 offset:20480
	s_waitcnt lgkmcnt(5)
	v_pk_fma_f32 v[248:249], v[236:237], v[20:21], v[248:249]
	v_pk_fma_f32 v[250:251], v[236:237], v[52:53], v[250:251]
	v_pk_fma_f32 v[248:249], v[238:239], v[18:19], v[248:249]
	v_pk_fma_f32 v[250:251], v[238:239], v[50:51], v[250:251]
	ds_read_b128 v[236:239], v110 offset:21504
	v_add_f32_e32 v83, v248, v249
	v_add_f32_e32 v84, v250, v251
	s_waitcnt lgkmcnt(5)
	v_pk_mul_f32 v[248:249], v[240:241], v[48:49]
	v_pk_mul_f32 v[250:251], v[240:241], v[72:73]
	v_pk_fma_f32 v[248:249], v[242:243], v[46:47], v[248:249]
	v_pk_fma_f32 v[250:251], v[242:243], v[70:71], v[250:251]
	ds_read_b128 v[240:243], v110 offset:22528
	s_waitcnt lgkmcnt(5)
	v_pk_fma_f32 v[248:249], v[244:245], v[44:45], v[248:249]
	v_pk_fma_f32 v[250:251], v[244:245], v[80:81], v[250:251]
	v_pk_fma_f32 v[248:249], v[246:247], v[42:43], v[248:249]
	v_pk_fma_f32 v[250:251], v[246:247], v[78:79], v[250:251]
	ds_read_b128 v[244:247], v110 offset:23552
	s_waitcnt lgkmcnt(5)
	v_pk_fma_f32 v[248:249], v[224:225], v[40:41], v[248:249]
	v_pk_fma_f32 v[250:251], v[224:225], v[76:77], v[250:251]
	v_pk_fma_f32 v[248:249], v[226:227], v[38:39], v[248:249]
	v_pk_fma_f32 v[250:251], v[226:227], v[74:75], v[250:251]
	ds_read_b128 v[224:227], v110 offset:24576
	s_waitcnt lgkmcnt(5)
	v_pk_fma_f32 v[248:249], v[228:229], v[32:33], v[248:249]
	v_pk_fma_f32 v[250:251], v[228:229], v[64:65], v[250:251]
	v_pk_fma_f32 v[248:249], v[230:231], v[30:31], v[248:249]
	v_pk_fma_f32 v[250:251], v[230:231], v[62:63], v[250:251]
	ds_read_b128 v[228:231], v110 offset:25600
	s_waitcnt lgkmcnt(5)
	v_pk_fma_f32 v[248:249], v[232:233], v[36:37], v[248:249]
	v_pk_fma_f32 v[250:251], v[232:233], v[68:69], v[250:251]
	v_pk_fma_f32 v[248:249], v[234:235], v[34:35], v[248:249]
	v_pk_fma_f32 v[250:251], v[234:235], v[66:67], v[250:251]
	ds_read_b128 v[232:235], v110 offset:26624
	s_waitcnt lgkmcnt(5)
	v_pk_fma_f32 v[248:249], v[236:237], v[28:29], v[248:249]
	v_pk_fma_f32 v[250:251], v[236:237], v[60:61], v[250:251]
	v_pk_fma_f32 v[248:249], v[238:239], v[26:27], v[248:249]
	v_pk_fma_f32 v[250:251], v[238:239], v[58:59], v[250:251]
	ds_read_b128 v[236:239], v110 offset:27648
	s_waitcnt lgkmcnt(5)
	v_pk_fma_f32 v[248:249], v[240:241], v[24:25], v[248:249]
	v_pk_fma_f32 v[250:251], v[240:241], v[56:57], v[250:251]
	v_pk_fma_f32 v[248:249], v[242:243], v[22:23], v[248:249]
	v_pk_fma_f32 v[250:251], v[242:243], v[54:55], v[250:251]
	ds_read_b128 v[240:243], v110 offset:28672
	s_waitcnt lgkmcnt(5)
	v_pk_fma_f32 v[248:249], v[244:245], v[20:21], v[248:249]
	v_pk_fma_f32 v[250:251], v[244:245], v[52:53], v[250:251]
	v_pk_fma_f32 v[248:249], v[246:247], v[18:19], v[248:249]
	v_pk_fma_f32 v[250:251], v[246:247], v[50:51], v[250:251]
	ds_read_b128 v[244:247], v110 offset:29696
	v_add_f32_e32 v85, v248, v249
	v_add_f32_e32 v86, v250, v251
	s_waitcnt lgkmcnt(5)
	v_pk_mul_f32 v[248:249], v[224:225], v[48:49]
	v_pk_mul_f32 v[250:251], v[224:225], v[72:73]
	v_pk_fma_f32 v[248:249], v[226:227], v[46:47], v[248:249]
	v_pk_fma_f32 v[250:251], v[226:227], v[70:71], v[250:251]
	ds_read_b128 v[224:227], v110 offset:30720
	s_waitcnt lgkmcnt(5)
	v_pk_fma_f32 v[248:249], v[228:229], v[44:45], v[248:249]
	v_pk_fma_f32 v[250:251], v[228:229], v[80:81], v[250:251]
	v_pk_fma_f32 v[248:249], v[230:231], v[42:43], v[248:249]
	v_pk_fma_f32 v[250:251], v[230:231], v[78:79], v[250:251]
	ds_read_b128 v[228:231], v110 offset:31744
	s_waitcnt lgkmcnt(5)
	v_pk_fma_f32 v[248:249], v[232:233], v[40:41], v[248:249]
	v_pk_fma_f32 v[250:251], v[232:233], v[76:77], v[250:251]
	v_pk_fma_f32 v[248:249], v[234:235], v[38:39], v[248:249]
	v_pk_fma_f32 v[250:251], v[234:235], v[74:75], v[250:251]
	ds_read_b128 v[232:235], v110 offset:32768
	s_waitcnt lgkmcnt(5)
	v_pk_fma_f32 v[248:249], v[236:237], v[32:33], v[248:249]
	v_pk_fma_f32 v[250:251], v[236:237], v[64:65], v[250:251]
	v_pk_fma_f32 v[248:249], v[238:239], v[30:31], v[248:249]
	v_pk_fma_f32 v[250:251], v[238:239], v[62:63], v[250:251]
	ds_read_b128 v[236:239], v110 offset:33792
	s_waitcnt lgkmcnt(5)
	v_pk_fma_f32 v[248:249], v[240:241], v[36:37], v[248:249]
	v_pk_fma_f32 v[250:251], v[240:241], v[68:69], v[250:251]
	v_pk_fma_f32 v[248:249], v[242:243], v[34:35], v[248:249]
	v_pk_fma_f32 v[250:251], v[242:243], v[66:67], v[250:251]
	ds_read_b128 v[240:243], v110 offset:34816
	s_waitcnt lgkmcnt(5)
	v_pk_fma_f32 v[248:249], v[244:245], v[28:29], v[248:249]
	v_pk_fma_f32 v[250:251], v[244:245], v[60:61], v[250:251]
	v_pk_fma_f32 v[248:249], v[246:247], v[26:27], v[248:249]
	v_pk_fma_f32 v[250:251], v[246:247], v[58:59], v[250:251]
	ds_read_b128 v[244:247], v110 offset:35840
	s_waitcnt lgkmcnt(5)
	v_pk_fma_f32 v[248:249], v[224:225], v[24:25], v[248:249]
	v_pk_fma_f32 v[250:251], v[224:225], v[56:57], v[250:251]
	v_pk_fma_f32 v[248:249], v[226:227], v[22:23], v[248:249]
	v_pk_fma_f32 v[250:251], v[226:227], v[54:55], v[250:251]
	ds_read_b128 v[224:227], v110 offset:36864
	s_waitcnt lgkmcnt(5)
	v_pk_fma_f32 v[248:249], v[228:229], v[20:21], v[248:249]
	v_pk_fma_f32 v[250:251], v[228:229], v[52:53], v[250:251]
	v_pk_fma_f32 v[248:249], v[230:231], v[18:19], v[248:249]
	v_pk_fma_f32 v[250:251], v[230:231], v[50:51], v[250:251]
	ds_read_b128 v[228:231], v110 offset:37888
	v_add_f32_e32 v87, v248, v249
	v_add_f32_e32 v88, v250, v251
	s_waitcnt lgkmcnt(5)
	v_pk_mul_f32 v[248:249], v[232:233], v[48:49]
	v_pk_mul_f32 v[250:251], v[232:233], v[72:73]
	v_pk_fma_f32 v[248:249], v[234:235], v[46:47], v[248:249]
	v_pk_fma_f32 v[250:251], v[234:235], v[70:71], v[250:251]
	ds_read_b128 v[232:235], v110 offset:38912
	s_waitcnt lgkmcnt(5)
	v_pk_fma_f32 v[248:249], v[236:237], v[44:45], v[248:249]
	v_pk_fma_f32 v[250:251], v[236:237], v[80:81], v[250:251]
	v_pk_fma_f32 v[248:249], v[238:239], v[42:43], v[248:249]
	v_pk_fma_f32 v[250:251], v[238:239], v[78:79], v[250:251]
	ds_read_b128 v[236:239], v110 offset:39936
	s_waitcnt lgkmcnt(5)
	v_pk_fma_f32 v[248:249], v[240:241], v[40:41], v[248:249]
	v_pk_fma_f32 v[250:251], v[240:241], v[76:77], v[250:251]
	v_pk_fma_f32 v[248:249], v[242:243], v[38:39], v[248:249]
	v_pk_fma_f32 v[250:251], v[242:243], v[74:75], v[250:251]
	ds_read_b128 v[240:243], v110 offset:40960
	s_waitcnt lgkmcnt(5)
	v_pk_fma_f32 v[248:249], v[244:245], v[32:33], v[248:249]
	v_pk_fma_f32 v[250:251], v[244:245], v[64:65], v[250:251]
	v_pk_fma_f32 v[248:249], v[246:247], v[30:31], v[248:249]
	v_pk_fma_f32 v[250:251], v[246:247], v[62:63], v[250:251]
	ds_read_b128 v[244:247], v110 offset:41984
	s_waitcnt lgkmcnt(5)
	v_pk_fma_f32 v[248:249], v[224:225], v[36:37], v[248:249]
	v_pk_fma_f32 v[250:251], v[224:225], v[68:69], v[250:251]
	v_pk_fma_f32 v[248:249], v[226:227], v[34:35], v[248:249]
	v_pk_fma_f32 v[250:251], v[226:227], v[66:67], v[250:251]
	ds_read_b128 v[224:227], v110 offset:43008
	s_waitcnt lgkmcnt(5)
	v_pk_fma_f32 v[248:249], v[228:229], v[28:29], v[248:249]
	v_pk_fma_f32 v[250:251], v[228:229], v[60:61], v[250:251]
	v_pk_fma_f32 v[248:249], v[230:231], v[26:27], v[248:249]
	v_pk_fma_f32 v[250:251], v[230:231], v[58:59], v[250:251]
	ds_read_b128 v[228:231], v110 offset:44032
	s_waitcnt lgkmcnt(5)
	v_pk_fma_f32 v[248:249], v[232:233], v[24:25], v[248:249]
	v_pk_fma_f32 v[250:251], v[232:233], v[56:57], v[250:251]
	v_pk_fma_f32 v[248:249], v[234:235], v[22:23], v[248:249]
	v_pk_fma_f32 v[250:251], v[234:235], v[54:55], v[250:251]
	ds_read_b128 v[232:235], v110 offset:45056
	s_waitcnt lgkmcnt(5)
	v_pk_fma_f32 v[248:249], v[236:237], v[20:21], v[248:249]
	v_pk_fma_f32 v[250:251], v[236:237], v[52:53], v[250:251]
	v_pk_fma_f32 v[248:249], v[238:239], v[18:19], v[248:249]
	v_pk_fma_f32 v[250:251], v[238:239], v[50:51], v[250:251]
	ds_read_b128 v[236:239], v110 offset:46080
	v_add_f32_e32 v89, v248, v249
	v_add_f32_e32 v90, v250, v251
	s_waitcnt lgkmcnt(5)
	v_pk_mul_f32 v[248:249], v[240:241], v[48:49]
	v_pk_mul_f32 v[250:251], v[240:241], v[72:73]
	v_pk_fma_f32 v[248:249], v[242:243], v[46:47], v[248:249]
	v_pk_fma_f32 v[250:251], v[242:243], v[70:71], v[250:251]
	ds_read_b128 v[240:243], v110 offset:47104
	s_waitcnt lgkmcnt(5)
	v_pk_fma_f32 v[248:249], v[244:245], v[44:45], v[248:249]
	v_pk_fma_f32 v[250:251], v[244:245], v[80:81], v[250:251]
	v_pk_fma_f32 v[248:249], v[246:247], v[42:43], v[248:249]
	v_pk_fma_f32 v[250:251], v[246:247], v[78:79], v[250:251]
	ds_read_b128 v[244:247], v110 offset:48128
	s_waitcnt lgkmcnt(5)
	v_pk_fma_f32 v[248:249], v[224:225], v[40:41], v[248:249]
	v_pk_fma_f32 v[250:251], v[224:225], v[76:77], v[250:251]
	v_pk_fma_f32 v[248:249], v[226:227], v[38:39], v[248:249]
	v_pk_fma_f32 v[250:251], v[226:227], v[74:75], v[250:251]
	ds_read_b128 v[224:227], v110 offset:49152
	s_waitcnt lgkmcnt(5)
	v_pk_fma_f32 v[248:249], v[228:229], v[32:33], v[248:249]
	v_pk_fma_f32 v[250:251], v[228:229], v[64:65], v[250:251]
	v_pk_fma_f32 v[248:249], v[230:231], v[30:31], v[248:249]
	v_pk_fma_f32 v[250:251], v[230:231], v[62:63], v[250:251]
	ds_read_b128 v[228:231], v110 offset:50176
	s_waitcnt lgkmcnt(5)
	v_pk_fma_f32 v[248:249], v[232:233], v[36:37], v[248:249]
	v_pk_fma_f32 v[250:251], v[232:233], v[68:69], v[250:251]
	v_pk_fma_f32 v[248:249], v[234:235], v[34:35], v[248:249]
	v_pk_fma_f32 v[250:251], v[234:235], v[66:67], v[250:251]
	ds_read_b128 v[232:235], v110 offset:51200
	s_waitcnt lgkmcnt(5)
	v_pk_fma_f32 v[248:249], v[236:237], v[28:29], v[248:249]
	v_pk_fma_f32 v[250:251], v[236:237], v[60:61], v[250:251]
	v_pk_fma_f32 v[248:249], v[238:239], v[26:27], v[248:249]
	v_pk_fma_f32 v[250:251], v[238:239], v[58:59], v[250:251]
	ds_read_b128 v[236:239], v110 offset:52224
	s_waitcnt lgkmcnt(5)
	v_pk_fma_f32 v[248:249], v[240:241], v[24:25], v[248:249]
	v_pk_fma_f32 v[250:251], v[240:241], v[56:57], v[250:251]
	v_pk_fma_f32 v[248:249], v[242:243], v[22:23], v[248:249]
	v_pk_fma_f32 v[250:251], v[242:243], v[54:55], v[250:251]
	ds_read_b128 v[240:243], v110 offset:53248
	s_waitcnt lgkmcnt(5)
	v_pk_fma_f32 v[248:249], v[244:245], v[20:21], v[248:249]
	v_pk_fma_f32 v[250:251], v[244:245], v[52:53], v[250:251]
	v_pk_fma_f32 v[248:249], v[246:247], v[18:19], v[248:249]
	v_pk_fma_f32 v[250:251], v[246:247], v[50:51], v[250:251]
	ds_read_b128 v[244:247], v110 offset:54272
	v_add_f32_e32 v91, v248, v249
	v_add_f32_e32 v92, v250, v251
	s_waitcnt lgkmcnt(5)
	v_pk_mul_f32 v[248:249], v[224:225], v[48:49]
	v_pk_mul_f32 v[250:251], v[224:225], v[72:73]
	v_pk_fma_f32 v[248:249], v[226:227], v[46:47], v[248:249]
	v_pk_fma_f32 v[250:251], v[226:227], v[70:71], v[250:251]
	ds_read_b128 v[224:227], v110 offset:55296
	s_waitcnt lgkmcnt(5)
	v_pk_fma_f32 v[248:249], v[228:229], v[44:45], v[248:249]
	v_pk_fma_f32 v[250:251], v[228:229], v[80:81], v[250:251]
	v_pk_fma_f32 v[248:249], v[230:231], v[42:43], v[248:249]
	v_pk_fma_f32 v[250:251], v[230:231], v[78:79], v[250:251]
	ds_read_b128 v[228:231], v110 offset:56320
	s_waitcnt lgkmcnt(5)
	v_pk_fma_f32 v[248:249], v[232:233], v[40:41], v[248:249]
	v_pk_fma_f32 v[250:251], v[232:233], v[76:77], v[250:251]
	v_pk_fma_f32 v[248:249], v[234:235], v[38:39], v[248:249]
	v_pk_fma_f32 v[250:251], v[234:235], v[74:75], v[250:251]
	ds_read_b128 v[232:235], v110 offset:57344
	s_waitcnt lgkmcnt(5)
	v_pk_fma_f32 v[248:249], v[236:237], v[32:33], v[248:249]
	v_pk_fma_f32 v[250:251], v[236:237], v[64:65], v[250:251]
	v_pk_fma_f32 v[248:249], v[238:239], v[30:31], v[248:249]
	v_pk_fma_f32 v[250:251], v[238:239], v[62:63], v[250:251]
	ds_read_b128 v[236:239], v110 offset:58368
	s_waitcnt lgkmcnt(5)
	v_pk_fma_f32 v[248:249], v[240:241], v[36:37], v[248:249]
	v_pk_fma_f32 v[250:251], v[240:241], v[68:69], v[250:251]
	v_pk_fma_f32 v[248:249], v[242:243], v[34:35], v[248:249]
	v_pk_fma_f32 v[250:251], v[242:243], v[66:67], v[250:251]
	ds_read_b128 v[240:243], v110 offset:59392
	s_waitcnt lgkmcnt(5)
	v_pk_fma_f32 v[248:249], v[244:245], v[28:29], v[248:249]
	v_pk_fma_f32 v[250:251], v[244:245], v[60:61], v[250:251]
	v_pk_fma_f32 v[248:249], v[246:247], v[26:27], v[248:249]
	v_pk_fma_f32 v[250:251], v[246:247], v[58:59], v[250:251]
	ds_read_b128 v[244:247], v110 offset:60416
	s_waitcnt lgkmcnt(5)
	v_pk_fma_f32 v[248:249], v[224:225], v[24:25], v[248:249]
	v_pk_fma_f32 v[250:251], v[224:225], v[56:57], v[250:251]
	v_pk_fma_f32 v[248:249], v[226:227], v[22:23], v[248:249]
	v_pk_fma_f32 v[250:251], v[226:227], v[54:55], v[250:251]
	ds_read_b128 v[224:227], v110 offset:61440
	s_waitcnt lgkmcnt(5)
	v_pk_fma_f32 v[248:249], v[228:229], v[20:21], v[248:249]
	v_pk_fma_f32 v[250:251], v[228:229], v[52:53], v[250:251]
	v_pk_fma_f32 v[248:249], v[230:231], v[18:19], v[248:249]
	v_pk_fma_f32 v[250:251], v[230:231], v[50:51], v[250:251]
	ds_read_b128 v[228:231], v110 offset:62464
	v_add_f32_e32 v93, v248, v249
	v_add_f32_e32 v94, v250, v251
	s_waitcnt lgkmcnt(5)
	v_pk_mul_f32 v[248:249], v[232:233], v[48:49]
	v_pk_mul_f32 v[250:251], v[232:233], v[72:73]
	v_pk_fma_f32 v[248:249], v[234:235], v[46:47], v[248:249]
	v_pk_fma_f32 v[250:251], v[234:235], v[70:71], v[250:251]
	ds_read_b128 v[232:235], v110 offset:63488
	s_waitcnt lgkmcnt(5)
	v_pk_fma_f32 v[248:249], v[236:237], v[44:45], v[248:249]
	v_pk_fma_f32 v[250:251], v[236:237], v[80:81], v[250:251]
	v_pk_fma_f32 v[248:249], v[238:239], v[42:43], v[248:249]
	v_pk_fma_f32 v[250:251], v[238:239], v[78:79], v[250:251]
	ds_read_b128 v[236:239], v110 offset:64512
	s_waitcnt lgkmcnt(5)
	v_pk_fma_f32 v[248:249], v[240:241], v[40:41], v[248:249]
	v_pk_fma_f32 v[250:251], v[240:241], v[76:77], v[250:251]
	v_pk_fma_f32 v[248:249], v[242:243], v[38:39], v[248:249]
	v_pk_fma_f32 v[250:251], v[242:243], v[74:75], v[250:251]
	ds_read_b128 v[240:243], v117
	s_waitcnt lgkmcnt(5)
	v_pk_fma_f32 v[248:249], v[244:245], v[32:33], v[248:249]
	v_pk_fma_f32 v[250:251], v[244:245], v[64:65], v[250:251]
	v_pk_fma_f32 v[248:249], v[246:247], v[30:31], v[248:249]
	v_pk_fma_f32 v[250:251], v[246:247], v[62:63], v[250:251]
	ds_read_b128 v[244:247], v118
	s_waitcnt lgkmcnt(5)
	v_pk_fma_f32 v[248:249], v[224:225], v[36:37], v[248:249]
	v_pk_fma_f32 v[250:251], v[224:225], v[68:69], v[250:251]
	v_pk_fma_f32 v[248:249], v[226:227], v[34:35], v[248:249]
	v_pk_fma_f32 v[250:251], v[226:227], v[66:67], v[250:251]
	ds_read_b128 v[224:227], v119
	s_waitcnt lgkmcnt(5)
	v_pk_fma_f32 v[248:249], v[228:229], v[28:29], v[248:249]
	v_pk_fma_f32 v[250:251], v[228:229], v[60:61], v[250:251]
	v_pk_fma_f32 v[248:249], v[230:231], v[26:27], v[248:249]
	v_pk_fma_f32 v[250:251], v[230:231], v[58:59], v[250:251]
	ds_read_b128 v[228:231], v120
	s_waitcnt lgkmcnt(5)
	v_pk_fma_f32 v[248:249], v[232:233], v[24:25], v[248:249]
	v_pk_fma_f32 v[250:251], v[232:233], v[56:57], v[250:251]
	v_pk_fma_f32 v[248:249], v[234:235], v[22:23], v[248:249]
	v_pk_fma_f32 v[250:251], v[234:235], v[54:55], v[250:251]
	ds_read_b128 v[232:235], v121
	s_waitcnt lgkmcnt(5)
	v_pk_fma_f32 v[248:249], v[236:237], v[20:21], v[248:249]
	v_pk_fma_f32 v[250:251], v[236:237], v[52:53], v[250:251]
	v_pk_fma_f32 v[248:249], v[238:239], v[18:19], v[248:249]
	v_pk_fma_f32 v[250:251], v[238:239], v[50:51], v[250:251]
	ds_read_b128 v[236:239], v122
	v_add_f32_e32 v95, v248, v249
	v_add_f32_e32 v96, v250, v251
	s_waitcnt lgkmcnt(5)
	v_pk_mul_f32 v[248:249], v[240:241], v[48:49]
	v_pk_mul_f32 v[250:251], v[240:241], v[72:73]
	v_pk_fma_f32 v[248:249], v[242:243], v[46:47], v[248:249]
	v_pk_fma_f32 v[250:251], v[242:243], v[70:71], v[250:251]
	ds_read_b128 v[240:243], v123
	s_waitcnt lgkmcnt(5)
	v_pk_fma_f32 v[248:249], v[244:245], v[44:45], v[248:249]
	v_pk_fma_f32 v[250:251], v[244:245], v[80:81], v[250:251]
	v_pk_fma_f32 v[248:249], v[246:247], v[42:43], v[248:249]
	v_pk_fma_f32 v[250:251], v[246:247], v[78:79], v[250:251]
	ds_read_b128 v[244:247], v124
	s_waitcnt lgkmcnt(5)
	v_pk_fma_f32 v[248:249], v[224:225], v[40:41], v[248:249]
	v_pk_fma_f32 v[250:251], v[224:225], v[76:77], v[250:251]
	v_pk_fma_f32 v[248:249], v[226:227], v[38:39], v[248:249]
	v_pk_fma_f32 v[250:251], v[226:227], v[74:75], v[250:251]
	ds_read_b128 v[224:227], v125
	s_waitcnt lgkmcnt(5)
	v_pk_fma_f32 v[248:249], v[228:229], v[32:33], v[248:249]
	v_pk_fma_f32 v[250:251], v[228:229], v[64:65], v[250:251]
	v_pk_fma_f32 v[248:249], v[230:231], v[30:31], v[248:249]
	v_pk_fma_f32 v[250:251], v[230:231], v[62:63], v[250:251]
	ds_read_b128 v[228:231], v126
	s_waitcnt lgkmcnt(5)
	v_pk_fma_f32 v[248:249], v[232:233], v[36:37], v[248:249]
	v_pk_fma_f32 v[250:251], v[232:233], v[68:69], v[250:251]
	v_pk_fma_f32 v[248:249], v[234:235], v[34:35], v[248:249]
	v_pk_fma_f32 v[250:251], v[234:235], v[66:67], v[250:251]
	ds_read_b128 v[232:235], v127
	s_waitcnt lgkmcnt(5)
	v_pk_fma_f32 v[248:249], v[236:237], v[28:29], v[248:249]
	v_pk_fma_f32 v[250:251], v[236:237], v[60:61], v[250:251]
	v_pk_fma_f32 v[248:249], v[238:239], v[26:27], v[248:249]
	v_pk_fma_f32 v[250:251], v[238:239], v[58:59], v[250:251]
	ds_read_b128 v[236:239], v128
	s_waitcnt lgkmcnt(5)
	v_pk_fma_f32 v[248:249], v[240:241], v[24:25], v[248:249]
	v_pk_fma_f32 v[250:251], v[240:241], v[56:57], v[250:251]
	v_pk_fma_f32 v[248:249], v[242:243], v[22:23], v[248:249]
	v_pk_fma_f32 v[250:251], v[242:243], v[54:55], v[250:251]
	ds_read_b128 v[240:243], v129
	s_waitcnt lgkmcnt(5)
	v_pk_fma_f32 v[248:249], v[244:245], v[20:21], v[248:249]
	v_pk_fma_f32 v[250:251], v[244:245], v[52:53], v[250:251]
	v_pk_fma_f32 v[248:249], v[246:247], v[18:19], v[248:249]
	v_pk_fma_f32 v[250:251], v[246:247], v[50:51], v[250:251]
	ds_read_b128 v[244:247], v130
	v_add_f32_e32 v4, v248, v249
	v_add_f32_e32 v5, v250, v251
	s_waitcnt lgkmcnt(5)
	v_pk_mul_f32 v[248:249], v[224:225], v[48:49]
	v_pk_mul_f32 v[250:251], v[224:225], v[72:73]
	v_pk_fma_f32 v[248:249], v[226:227], v[46:47], v[248:249]
	v_pk_fma_f32 v[250:251], v[226:227], v[70:71], v[250:251]
	ds_read_b128 v[224:227], v131
	s_waitcnt lgkmcnt(5)
	v_pk_fma_f32 v[248:249], v[228:229], v[44:45], v[248:249]
	v_pk_fma_f32 v[250:251], v[228:229], v[80:81], v[250:251]
	v_pk_fma_f32 v[248:249], v[230:231], v[42:43], v[248:249]
	v_pk_fma_f32 v[250:251], v[230:231], v[78:79], v[250:251]
	ds_read_b128 v[228:231], v132
	s_waitcnt lgkmcnt(5)
	v_pk_fma_f32 v[248:249], v[232:233], v[40:41], v[248:249]
	v_pk_fma_f32 v[250:251], v[232:233], v[76:77], v[250:251]
	v_pk_fma_f32 v[248:249], v[234:235], v[38:39], v[248:249]
	v_pk_fma_f32 v[250:251], v[234:235], v[74:75], v[250:251]
	ds_read_b128 v[232:235], v133
	s_waitcnt lgkmcnt(5)
	v_pk_fma_f32 v[248:249], v[236:237], v[32:33], v[248:249]
	v_pk_fma_f32 v[250:251], v[236:237], v[64:65], v[250:251]
	v_pk_fma_f32 v[248:249], v[238:239], v[30:31], v[248:249]
	v_pk_fma_f32 v[250:251], v[238:239], v[62:63], v[250:251]
	ds_read_b128 v[236:239], v134
	s_waitcnt lgkmcnt(5)
	v_pk_fma_f32 v[248:249], v[240:241], v[36:37], v[248:249]
	v_pk_fma_f32 v[250:251], v[240:241], v[68:69], v[250:251]
	v_pk_fma_f32 v[248:249], v[242:243], v[34:35], v[248:249]
	v_pk_fma_f32 v[250:251], v[242:243], v[66:67], v[250:251]
	ds_read_b128 v[240:243], v135
	s_waitcnt lgkmcnt(5)
	v_pk_fma_f32 v[248:249], v[244:245], v[28:29], v[248:249]
	v_pk_fma_f32 v[250:251], v[244:245], v[60:61], v[250:251]
	v_pk_fma_f32 v[248:249], v[246:247], v[26:27], v[248:249]
	v_pk_fma_f32 v[250:251], v[246:247], v[58:59], v[250:251]
	ds_read_b128 v[244:247], v136
	s_waitcnt lgkmcnt(5)
	v_pk_fma_f32 v[248:249], v[224:225], v[24:25], v[248:249]
	v_pk_fma_f32 v[250:251], v[224:225], v[56:57], v[250:251]
	v_pk_fma_f32 v[248:249], v[226:227], v[22:23], v[248:249]
	v_pk_fma_f32 v[250:251], v[226:227], v[54:55], v[250:251]
	ds_read_b128 v[224:227], v137
	s_waitcnt lgkmcnt(5)
	v_pk_fma_f32 v[248:249], v[228:229], v[20:21], v[248:249]
	v_pk_fma_f32 v[250:251], v[228:229], v[52:53], v[250:251]
	v_pk_fma_f32 v[248:249], v[230:231], v[18:19], v[248:249]
	v_pk_fma_f32 v[250:251], v[230:231], v[50:51], v[250:251]
	ds_read_b128 v[228:231], v138
	v_add_f32_e32 v6, v248, v249
	v_add_f32_e32 v7, v250, v251
	s_waitcnt lgkmcnt(5)
	v_pk_mul_f32 v[248:249], v[232:233], v[48:49]
	v_pk_mul_f32 v[250:251], v[232:233], v[72:73]
	v_pk_fma_f32 v[248:249], v[234:235], v[46:47], v[248:249]
	v_pk_fma_f32 v[250:251], v[234:235], v[70:71], v[250:251]
	ds_read_b128 v[232:235], v139
	s_waitcnt lgkmcnt(5)
	v_pk_fma_f32 v[248:249], v[236:237], v[44:45], v[248:249]
	v_pk_fma_f32 v[250:251], v[236:237], v[80:81], v[250:251]
	v_pk_fma_f32 v[248:249], v[238:239], v[42:43], v[248:249]
	v_pk_fma_f32 v[250:251], v[238:239], v[78:79], v[250:251]
	ds_read_b128 v[236:239], v140
	s_waitcnt lgkmcnt(5)
	v_pk_fma_f32 v[248:249], v[240:241], v[40:41], v[248:249]
	v_pk_fma_f32 v[250:251], v[240:241], v[76:77], v[250:251]
	v_pk_fma_f32 v[248:249], v[242:243], v[38:39], v[248:249]
	v_pk_fma_f32 v[250:251], v[242:243], v[74:75], v[250:251]
	ds_read_b128 v[240:243], v141
	s_waitcnt lgkmcnt(5)
	v_pk_fma_f32 v[248:249], v[244:245], v[32:33], v[248:249]
	v_pk_fma_f32 v[250:251], v[244:245], v[64:65], v[250:251]
	v_pk_fma_f32 v[248:249], v[246:247], v[30:31], v[248:249]
	v_pk_fma_f32 v[250:251], v[246:247], v[62:63], v[250:251]
	ds_read_b128 v[244:247], v142
	s_waitcnt lgkmcnt(5)
	v_pk_fma_f32 v[248:249], v[224:225], v[36:37], v[248:249]
	v_pk_fma_f32 v[250:251], v[224:225], v[68:69], v[250:251]
	v_pk_fma_f32 v[248:249], v[226:227], v[34:35], v[248:249]
	v_pk_fma_f32 v[250:251], v[226:227], v[66:67], v[250:251]
	ds_read_b128 v[224:227], v143
	s_waitcnt lgkmcnt(5)
	v_pk_fma_f32 v[248:249], v[228:229], v[28:29], v[248:249]
	v_pk_fma_f32 v[250:251], v[228:229], v[60:61], v[250:251]
	v_pk_fma_f32 v[248:249], v[230:231], v[26:27], v[248:249]
	v_pk_fma_f32 v[250:251], v[230:231], v[58:59], v[250:251]
	ds_read_b128 v[228:231], v144
	s_waitcnt lgkmcnt(5)
	v_pk_fma_f32 v[248:249], v[232:233], v[24:25], v[248:249]
	v_pk_fma_f32 v[250:251], v[232:233], v[56:57], v[250:251]
	v_pk_fma_f32 v[248:249], v[234:235], v[22:23], v[248:249]
	v_pk_fma_f32 v[250:251], v[234:235], v[54:55], v[250:251]
	ds_read_b128 v[232:235], v145
	s_waitcnt lgkmcnt(5)
	v_pk_fma_f32 v[248:249], v[236:237], v[20:21], v[248:249]
	v_pk_fma_f32 v[250:251], v[236:237], v[52:53], v[250:251]
	v_pk_fma_f32 v[248:249], v[238:239], v[18:19], v[248:249]
	v_pk_fma_f32 v[250:251], v[238:239], v[50:51], v[250:251]
	ds_read_b128 v[236:239], v146
	v_add_f32_e32 v97, v248, v249
	v_add_f32_e32 v98, v250, v251
	s_waitcnt lgkmcnt(5)
	v_pk_mul_f32 v[248:249], v[240:241], v[48:49]
	v_pk_mul_f32 v[250:251], v[240:241], v[72:73]
	v_pk_fma_f32 v[248:249], v[242:243], v[46:47], v[248:249]
	v_pk_fma_f32 v[250:251], v[242:243], v[70:71], v[250:251]
	ds_read_b128 v[240:243], v147
	s_waitcnt lgkmcnt(5)
	v_pk_fma_f32 v[248:249], v[244:245], v[44:45], v[248:249]
	v_pk_fma_f32 v[250:251], v[244:245], v[80:81], v[250:251]
	v_pk_fma_f32 v[248:249], v[246:247], v[42:43], v[248:249]
	v_pk_fma_f32 v[250:251], v[246:247], v[78:79], v[250:251]
	ds_read_b128 v[244:247], v148
	s_waitcnt lgkmcnt(5)
	v_pk_fma_f32 v[248:249], v[224:225], v[40:41], v[248:249]
	v_pk_fma_f32 v[250:251], v[224:225], v[76:77], v[250:251]
	v_pk_fma_f32 v[248:249], v[226:227], v[38:39], v[248:249]
	v_pk_fma_f32 v[250:251], v[226:227], v[74:75], v[250:251]
	ds_read_b128 v[224:227], v149
	s_waitcnt lgkmcnt(5)
	v_pk_fma_f32 v[248:249], v[228:229], v[32:33], v[248:249]
	v_pk_fma_f32 v[250:251], v[228:229], v[64:65], v[250:251]
	v_pk_fma_f32 v[248:249], v[230:231], v[30:31], v[248:249]
	v_pk_fma_f32 v[250:251], v[230:231], v[62:63], v[250:251]
	ds_read_b128 v[228:231], v150
	s_waitcnt lgkmcnt(5)
	v_pk_fma_f32 v[248:249], v[232:233], v[36:37], v[248:249]
	v_pk_fma_f32 v[250:251], v[232:233], v[68:69], v[250:251]
	v_pk_fma_f32 v[248:249], v[234:235], v[34:35], v[248:249]
	v_pk_fma_f32 v[250:251], v[234:235], v[66:67], v[250:251]
	ds_read_b128 v[232:235], v151
	s_waitcnt lgkmcnt(5)
	v_pk_fma_f32 v[248:249], v[236:237], v[28:29], v[248:249]
	v_pk_fma_f32 v[250:251], v[236:237], v[60:61], v[250:251]
	v_pk_fma_f32 v[248:249], v[238:239], v[26:27], v[248:249]
	v_pk_fma_f32 v[250:251], v[238:239], v[58:59], v[250:251]
	ds_read_b128 v[236:239], v152
	s_waitcnt lgkmcnt(5)
	v_pk_fma_f32 v[248:249], v[240:241], v[24:25], v[248:249]
	v_pk_fma_f32 v[250:251], v[240:241], v[56:57], v[250:251]
	v_pk_fma_f32 v[248:249], v[242:243], v[22:23], v[248:249]
	v_pk_fma_f32 v[250:251], v[242:243], v[54:55], v[250:251]
	ds_read_b128 v[240:243], v153
	s_waitcnt lgkmcnt(5)
	v_pk_fma_f32 v[248:249], v[244:245], v[20:21], v[248:249]
	v_pk_fma_f32 v[250:251], v[244:245], v[52:53], v[250:251]
	v_pk_fma_f32 v[248:249], v[246:247], v[18:19], v[248:249]
	v_pk_fma_f32 v[250:251], v[246:247], v[50:51], v[250:251]
	ds_read_b128 v[244:247], v154
	v_add_f32_e32 v99, v248, v249
	v_add_f32_e32 v100, v250, v251
	s_waitcnt lgkmcnt(5)
	v_pk_mul_f32 v[248:249], v[224:225], v[48:49]
	v_pk_mul_f32 v[250:251], v[224:225], v[72:73]
	v_pk_fma_f32 v[248:249], v[226:227], v[46:47], v[248:249]
	v_pk_fma_f32 v[250:251], v[226:227], v[70:71], v[250:251]
	ds_read_b128 v[224:227], v155
	s_waitcnt lgkmcnt(5)
	v_pk_fma_f32 v[248:249], v[228:229], v[44:45], v[248:249]
	v_pk_fma_f32 v[250:251], v[228:229], v[80:81], v[250:251]
	v_pk_fma_f32 v[248:249], v[230:231], v[42:43], v[248:249]
	v_pk_fma_f32 v[250:251], v[230:231], v[78:79], v[250:251]
	ds_read_b128 v[228:231], v156
	s_waitcnt lgkmcnt(5)
	v_pk_fma_f32 v[248:249], v[232:233], v[40:41], v[248:249]
	v_pk_fma_f32 v[250:251], v[232:233], v[76:77], v[250:251]
	v_pk_fma_f32 v[248:249], v[234:235], v[38:39], v[248:249]
	v_pk_fma_f32 v[250:251], v[234:235], v[74:75], v[250:251]
	ds_read_b128 v[232:235], v157
	s_waitcnt lgkmcnt(5)
	v_pk_fma_f32 v[248:249], v[236:237], v[32:33], v[248:249]
	v_pk_fma_f32 v[250:251], v[236:237], v[64:65], v[250:251]
	v_pk_fma_f32 v[248:249], v[238:239], v[30:31], v[248:249]
	v_pk_fma_f32 v[250:251], v[238:239], v[62:63], v[250:251]
	ds_read_b128 v[236:239], v158
	s_waitcnt lgkmcnt(5)
	v_pk_fma_f32 v[248:249], v[240:241], v[36:37], v[248:249]
	v_pk_fma_f32 v[250:251], v[240:241], v[68:69], v[250:251]
	v_pk_fma_f32 v[248:249], v[242:243], v[34:35], v[248:249]
	v_pk_fma_f32 v[250:251], v[242:243], v[66:67], v[250:251]
	ds_read_b128 v[240:243], v159
	s_waitcnt lgkmcnt(5)
	v_pk_fma_f32 v[248:249], v[244:245], v[28:29], v[248:249]
	v_pk_fma_f32 v[250:251], v[244:245], v[60:61], v[250:251]
	v_pk_fma_f32 v[248:249], v[246:247], v[26:27], v[248:249]
	v_pk_fma_f32 v[250:251], v[246:247], v[58:59], v[250:251]
	ds_read_b128 v[244:247], v160
	s_waitcnt lgkmcnt(5)
	v_pk_fma_f32 v[248:249], v[224:225], v[24:25], v[248:249]
	v_pk_fma_f32 v[250:251], v[224:225], v[56:57], v[250:251]
	v_pk_fma_f32 v[248:249], v[226:227], v[22:23], v[248:249]
	v_pk_fma_f32 v[250:251], v[226:227], v[54:55], v[250:251]
	ds_read_b128 v[224:227], v161
	s_waitcnt lgkmcnt(5)
	v_pk_fma_f32 v[248:249], v[228:229], v[20:21], v[248:249]
	v_pk_fma_f32 v[250:251], v[228:229], v[52:53], v[250:251]
	v_pk_fma_f32 v[248:249], v[230:231], v[18:19], v[248:249]
	v_pk_fma_f32 v[250:251], v[230:231], v[50:51], v[250:251]
	ds_read_b128 v[228:231], v162
	v_add_f32_e32 v101, v248, v249
	v_add_f32_e32 v102, v250, v251
	s_waitcnt lgkmcnt(5)
	v_pk_mul_f32 v[248:249], v[232:233], v[48:49]
	v_pk_mul_f32 v[250:251], v[232:233], v[72:73]
	v_pk_fma_f32 v[248:249], v[234:235], v[46:47], v[248:249]
	v_pk_fma_f32 v[250:251], v[234:235], v[70:71], v[250:251]
	ds_read_b128 v[232:235], v163
	s_waitcnt lgkmcnt(5)
	v_pk_fma_f32 v[248:249], v[236:237], v[44:45], v[248:249]
	v_pk_fma_f32 v[250:251], v[236:237], v[80:81], v[250:251]
	v_pk_fma_f32 v[248:249], v[238:239], v[42:43], v[248:249]
	v_pk_fma_f32 v[250:251], v[238:239], v[78:79], v[250:251]
	ds_read_b128 v[236:239], v164
	s_waitcnt lgkmcnt(5)
	v_pk_fma_f32 v[248:249], v[240:241], v[40:41], v[248:249]
	v_pk_fma_f32 v[250:251], v[240:241], v[76:77], v[250:251]
	v_pk_fma_f32 v[248:249], v[242:243], v[38:39], v[248:249]
	v_pk_fma_f32 v[250:251], v[242:243], v[74:75], v[250:251]
	s_waitcnt lgkmcnt(4)
	v_pk_fma_f32 v[248:249], v[244:245], v[32:33], v[248:249]
	v_pk_fma_f32 v[250:251], v[244:245], v[64:65], v[250:251]
	v_pk_fma_f32 v[248:249], v[246:247], v[30:31], v[248:249]
	v_pk_fma_f32 v[250:251], v[246:247], v[62:63], v[250:251]
	s_waitcnt lgkmcnt(3)
	v_pk_fma_f32 v[248:249], v[224:225], v[36:37], v[248:249]
	v_pk_fma_f32 v[250:251], v[224:225], v[68:69], v[250:251]
	v_pk_fma_f32 v[248:249], v[226:227], v[34:35], v[248:249]
	v_pk_fma_f32 v[250:251], v[226:227], v[66:67], v[250:251]
	s_waitcnt lgkmcnt(2)
	v_pk_fma_f32 v[248:249], v[228:229], v[28:29], v[248:249]
	v_pk_fma_f32 v[250:251], v[228:229], v[60:61], v[250:251]
	v_pk_fma_f32 v[248:249], v[230:231], v[26:27], v[248:249]
	v_pk_fma_f32 v[250:251], v[230:231], v[58:59], v[250:251]
	s_waitcnt lgkmcnt(1)
	v_pk_fma_f32 v[248:249], v[232:233], v[24:25], v[248:249]
	v_pk_fma_f32 v[250:251], v[232:233], v[56:57], v[250:251]
	v_pk_fma_f32 v[248:249], v[234:235], v[22:23], v[248:249]
	v_pk_fma_f32 v[250:251], v[234:235], v[54:55], v[250:251]
	s_waitcnt lgkmcnt(0)
	v_pk_fma_f32 v[248:249], v[236:237], v[20:21], v[248:249]
	v_pk_fma_f32 v[250:251], v[236:237], v[52:53], v[250:251]
	v_pk_fma_f32 v[248:249], v[238:239], v[18:19], v[248:249]
	v_pk_fma_f32 v[250:251], v[238:239], v[50:51], v[250:251]
	v_add_f32_e32 v103, v248, v249
	v_add_f32_e32 v104, v250, v251
	ds_read_b128 v[224:227], v165
	ds_read_b128 v[106:109], v166
	ds_read_b128 v[240:243], v167
	ds_read_b128 v[236:239], v168
	ds_read_b128 v[232:235], v169
	ds_read_b128 v[228:231], v170
	s_waitcnt lgkmcnt(5)
	v_mul_f32_e32 v105, v225, v49
	v_mul_f32_e32 v225, v225, v73
	v_fmac_f32_e32 v105, v224, v48
	v_fmac_f32_e32 v225, v224, v72
	v_mul_f32_e32 v224, v227, v71
	v_mul_f32_e32 v191, v227, v47
	v_fmac_f32_e32 v224, v226, v70
	v_fmac_f32_e32 v191, v226, v46
	v_add_f32_e32 v224, v225, v224
	v_add_f32_e32 v105, v105, v191
	v_add_f32_e32 v191, 0, v224
	ds_read_b128 v[224:227], v171
	v_add_f32_e32 v105, 0, v105
	s_waitcnt lgkmcnt(5)
	v_mul_f32_e32 v192, v107, v45
	v_mul_f32_e32 v107, v107, v81
	v_fmac_f32_e32 v192, v106, v44
	v_fmac_f32_e32 v107, v106, v80
	v_mul_f32_e32 v106, v109, v79
	v_fmac_f32_e32 v106, v108, v78
	v_mul_f32_e32 v193, v109, v43
	v_add_f32_e32 v106, v107, v106
	v_fmac_f32_e32 v193, v108, v42
	v_add_f32_e32 v191, v191, v106
	ds_read_b128 v[106:109], v172
	v_add_f32_e32 v192, v192, v193
	v_add_f32_e32 v105, v105, v192
	s_waitcnt lgkmcnt(5)
	v_mul_f32_e32 v192, v241, v41
	v_mul_f32_e32 v241, v241, v77
	v_fmac_f32_e32 v192, v240, v40
	v_fmac_f32_e32 v241, v240, v76
	v_mul_f32_e32 v240, v243, v75
	v_fmac_f32_e32 v240, v242, v74
	v_mul_f32_e32 v193, v243, v39
	v_add_f32_e32 v240, v241, v240
	v_fmac_f32_e32 v193, v242, v38
	v_add_f32_e32 v191, v191, v240
	v_add_f32_e32 v192, v192, v193
	v_add_f32_e32 v105, v105, v192
	s_waitcnt lgkmcnt(4)
	v_mul_f32_e32 v192, v237, v33
	v_mul_f32_e32 v237, v237, v65
	v_fmac_f32_e32 v192, v236, v32
	v_fmac_f32_e32 v237, v236, v64
	v_mul_f32_e32 v236, v239, v63
	v_fmac_f32_e32 v236, v238, v62
	v_mul_f32_e32 v193, v239, v31
	v_add_f32_e32 v236, v237, v236
	v_fmac_f32_e32 v193, v238, v30
	v_add_f32_e32 v191, v191, v236
	v_add_f32_e32 v192, v192, v193
	v_add_f32_e32 v105, v105, v192
	s_waitcnt lgkmcnt(3)
	v_mul_f32_e32 v192, v233, v37
	v_mul_f32_e32 v233, v233, v69
	v_fmac_f32_e32 v192, v232, v36
	v_fmac_f32_e32 v233, v232, v68
	v_mul_f32_e32 v232, v235, v67
	v_fmac_f32_e32 v232, v234, v66
	v_mul_f32_e32 v193, v235, v35
	v_add_f32_e32 v232, v233, v232
	v_fmac_f32_e32 v193, v234, v34
	v_add_f32_e32 v191, v191, v232
	v_add_f32_e32 v192, v192, v193
	v_add_f32_e32 v105, v105, v192
	s_waitcnt lgkmcnt(2)
	v_mul_f32_e32 v192, v229, v29
	v_mul_f32_e32 v229, v229, v61
	v_fmac_f32_e32 v192, v228, v28
	v_fmac_f32_e32 v229, v228, v60
	v_mul_f32_e32 v228, v231, v59
	v_fmac_f32_e32 v228, v230, v58
	v_mul_f32_e32 v193, v231, v27
	v_add_f32_e32 v228, v229, v228
	v_fmac_f32_e32 v193, v230, v26
	v_add_f32_e32 v191, v191, v228
	v_add_f32_e32 v192, v192, v193
	v_add_f32_e32 v105, v105, v192
	s_waitcnt lgkmcnt(1)
	v_mul_f32_e32 v192, v225, v25
	v_mul_f32_e32 v225, v225, v57
	v_fmac_f32_e32 v192, v224, v24
	v_fmac_f32_e32 v225, v224, v56
	v_mul_f32_e32 v224, v227, v55
	v_fmac_f32_e32 v224, v226, v54
	v_mul_f32_e32 v193, v227, v23
	v_add_f32_e32 v224, v225, v224
	v_fmac_f32_e32 v193, v226, v22
	v_add_f32_e32 v191, v191, v224
	v_add_f32_e32 v192, v192, v193
	v_add_f32_e32 v105, v105, v192
	s_waitcnt lgkmcnt(0)
	v_mul_f32_e32 v192, v107, v21
	v_mul_f32_e32 v193, v109, v19
	v_fmac_f32_e32 v192, v106, v20
	v_fmac_f32_e32 v193, v108, v18
	v_add_f32_e32 v192, v192, v193
	v_add_f32_e32 v105, v105, v192
	ds_read_b128 v[192:195], v173
	v_mul_f32_e32 v107, v107, v53
	v_fmac_f32_e32 v107, v106, v52
	v_mul_f32_e32 v106, v109, v51
	v_fmac_f32_e32 v106, v108, v50
	s_waitcnt lgkmcnt(0)
	v_mul_f32_e32 v49, v193, v49
	v_mul_f32_e32 v47, v195, v47
	v_fmac_f32_e32 v49, v192, v48
	v_fmac_f32_e32 v47, v194, v46
	v_add_f32_e32 v46, v49, v47
	v_add_f32_e32 v106, v107, v106
	v_add_f32_e32 v107, 0, v46
	v_mul_f32_e32 v46, v193, v73
	v_mul_f32_e32 v47, v195, v71
	v_fmac_f32_e32 v46, v192, v72
	v_fmac_f32_e32 v47, v194, v70
	v_add_f32_e32 v46, v46, v47
	v_add_f32_e32 v70, 0, v46
	ds_read_b128 v[46:49], v174
	v_add_f32_e32 v106, v191, v106
	s_waitcnt lgkmcnt(0)
	v_mul_f32_e32 v45, v47, v45
	v_mul_f32_e32 v43, v49, v43
	v_fmac_f32_e32 v45, v46, v44
	v_fmac_f32_e32 v43, v48, v42
	v_add_f32_e32 v42, v45, v43
	v_add_f32_e32 v71, v107, v42
	v_mul_f32_e32 v42, v47, v81
	v_mul_f32_e32 v43, v49, v79
	v_fmac_f32_e32 v42, v46, v80
	v_fmac_f32_e32 v43, v48, v78
	v_add_f32_e32 v42, v42, v43
	v_add_f32_e32 v46, v70, v42
	ds_read_b128 v[42:45], v175
	s_waitcnt lgkmcnt(0)
	v_mul_f32_e32 v41, v43, v41
	v_mul_f32_e32 v39, v45, v39
	v_fmac_f32_e32 v41, v42, v40
	v_fmac_f32_e32 v39, v44, v38
	v_add_f32_e32 v38, v41, v39
	v_add_f32_e32 v47, v71, v38
	v_mul_f32_e32 v38, v43, v77
	v_mul_f32_e32 v39, v45, v75
	v_fmac_f32_e32 v38, v42, v76
	v_fmac_f32_e32 v39, v44, v74
	v_add_f32_e32 v38, v38, v39
	v_add_f32_e32 v42, v46, v38
	ds_read_b128 v[38:41], v176
	s_waitcnt lgkmcnt(0)
	v_mul_f32_e32 v33, v39, v33
	v_mul_f32_e32 v31, v41, v31
	v_fmac_f32_e32 v33, v38, v32
	v_fmac_f32_e32 v31, v40, v30
	v_add_f32_e32 v30, v33, v31
	v_add_f32_e32 v43, v47, v30
	v_mul_f32_e32 v30, v39, v65
	v_mul_f32_e32 v31, v41, v63
	v_fmac_f32_e32 v30, v38, v64
	v_fmac_f32_e32 v31, v40, v62
	v_add_f32_e32 v30, v30, v31
	v_add_f32_e32 v38, v42, v30
	ds_read_b128 v[224:227], v177
	ds_read_b128 v[30:33], v178
	s_waitcnt lgkmcnt(1)
	v_mul_f32_e32 v37, v225, v37
	v_mul_f32_e32 v225, v225, v69
	v_fmac_f32_e32 v37, v224, v36
	v_fmac_f32_e32 v225, v224, v68
	v_mul_f32_e32 v224, v227, v67
	v_mul_f32_e32 v35, v227, v35
	v_fmac_f32_e32 v224, v226, v66
	v_fmac_f32_e32 v35, v226, v34
	v_add_f32_e32 v224, v225, v224
	v_add_f32_e32 v34, v37, v35
	v_add_f32_e32 v35, v38, v224
	v_add_f32_e32 v34, v43, v34
	s_waitcnt lgkmcnt(0)
	v_mul_f32_e32 v29, v31, v29
	v_mul_f32_e32 v27, v33, v27
	v_fmac_f32_e32 v29, v30, v28
	v_fmac_f32_e32 v27, v32, v26
	v_add_f32_e32 v26, v29, v27
	v_add_f32_e32 v34, v34, v26
	v_mul_f32_e32 v26, v31, v61
	v_mul_f32_e32 v27, v33, v59
	v_fmac_f32_e32 v26, v30, v60
	v_fmac_f32_e32 v27, v32, v58
	v_add_f32_e32 v26, v26, v27
	v_add_f32_e32 v30, v35, v26
	ds_read_b128 v[26:29], v179
	s_waitcnt lgkmcnt(0)
	v_mul_f32_e32 v25, v27, v25
	v_mul_f32_e32 v23, v29, v23
	v_fmac_f32_e32 v25, v26, v24
	v_fmac_f32_e32 v23, v28, v22
	v_add_f32_e32 v22, v25, v23
	v_add_f32_e32 v31, v34, v22
	v_mul_f32_e32 v22, v27, v57
	v_mul_f32_e32 v23, v29, v55
	v_fmac_f32_e32 v22, v26, v56
	v_fmac_f32_e32 v23, v28, v54
	v_add_f32_e32 v22, v22, v23
	v_add_f32_e32 v26, v30, v22
	ds_read_b128 v[22:25], v180
	v_cndmask_b32_e64 v27, v92, v104, s[34:35]
	v_cndmask_b32_e64 v28, v104, v92, s[34:35]
	v_cndmask_b32_e64 v29, v94, v106, s[34:35]
	v_cndmask_b32_e64 v30, v106, v94, s[34:35]
	s_waitcnt lgkmcnt(0)
	v_mul_f32_e32 v21, v23, v21
	v_mul_f32_e32 v19, v25, v19
	v_fmac_f32_e32 v21, v22, v20
	v_fmac_f32_e32 v19, v24, v18
	v_add_f32_e32 v18, v21, v19
	v_mul_f32_e32 v19, v23, v53
	v_mul_f32_e32 v20, v25, v51
	v_fmac_f32_e32 v19, v22, v52
	v_fmac_f32_e32 v20, v24, v50
	v_add_f32_e32 v19, v19, v20
	v_cndmask_b32_e64 v20, v2, v4, s[34:35]
	v_cndmask_b32_e64 v2, v4, v2, s[34:35]
	v_cndmask_b32_e64 v4, v82, v5, s[34:35]
	ds_bpermute_b32 v4, v112, v4
	v_cndmask_b32_e64 v5, v5, v82, s[34:35]
	ds_bpermute_b32 v20, v112, v20
	v_cndmask_b32_e64 v21, v86, v98, s[34:35]
	v_cndmask_b32_e64 v22, v98, v86, s[34:35]
	s_waitcnt lgkmcnt(1)
	v_add_f32_e32 v4, v5, v4
	v_cndmask_b32_e64 v5, v83, v6, s[34:35]
	ds_bpermute_b32 v5, v112, v5
	s_waitcnt lgkmcnt(1)
	v_add_f32_e32 v2, v2, v20
	v_cndmask_b32_e64 v6, v6, v83, s[34:35]
	v_cndmask_b32_e64 v20, v84, v7, s[34:35]
	v_cndmask_b32_e64 v7, v7, v84, s[34:35]
	s_waitcnt lgkmcnt(0)
	v_add_f32_e32 v5, v6, v5
	ds_bpermute_b32 v6, v112, v20
	v_cndmask_b32_e64 v20, v97, v85, s[34:35]
	v_cndmask_b32_e64 v23, v88, v100, s[34:35]
	v_cndmask_b32_e64 v24, v100, v88, s[34:35]
	v_cndmask_b32_e64 v25, v90, v102, s[34:35]
	s_waitcnt lgkmcnt(0)
	v_add_f32_e32 v6, v7, v6
	v_cndmask_b32_e64 v7, v85, v97, s[34:35]
	ds_bpermute_b32 v7, v112, v7
	v_add_f32_e32 v19, v26, v19
	v_cndmask_b32_e64 v26, v102, v90, s[34:35]
	v_add_f32_e32 v18, v31, v18
	s_waitcnt lgkmcnt(0)
	v_add_f32_e32 v7, v20, v7
	ds_bpermute_b32 v20, v112, v21
	v_cndmask_b32_e64 v21, v87, v99, s[34:35]
	ds_bpermute_b32 v21, v112, v21
	s_waitcnt lgkmcnt(1)
	v_add_f32_e32 v20, v22, v20
	v_cndmask_b32_e64 v22, v99, v87, s[34:35]
	s_waitcnt lgkmcnt(0)
	v_add_f32_e32 v21, v22, v21
	ds_bpermute_b32 v22, v112, v23
	v_cndmask_b32_e64 v23, v89, v101, s[34:35]
	ds_bpermute_b32 v23, v112, v23
	s_waitcnt lgkmcnt(1)
	v_add_f32_e32 v22, v24, v22
	v_cndmask_b32_e64 v24, v101, v89, s[34:35]
	s_waitcnt lgkmcnt(0)
	v_add_f32_e32 v23, v24, v23
	ds_bpermute_b32 v24, v112, v25
	v_cndmask_b32_e64 v25, v91, v103, s[34:35]
	ds_bpermute_b32 v25, v112, v25
	s_waitcnt lgkmcnt(1)
	v_add_f32_e32 v24, v26, v24
	v_cndmask_b32_e64 v26, v103, v91, s[34:35]
	s_waitcnt lgkmcnt(0)
	v_add_f32_e32 v25, v26, v25
	ds_bpermute_b32 v26, v112, v27
	v_cndmask_b32_e64 v27, v93, v105, s[34:35]
	ds_bpermute_b32 v27, v112, v27
	s_waitcnt lgkmcnt(1)
	v_add_f32_e32 v26, v28, v26
	v_cndmask_b32_e64 v28, v105, v93, s[34:35]
	s_waitcnt lgkmcnt(0)
	v_add_f32_e32 v27, v28, v27
	ds_bpermute_b32 v28, v112, v29
	v_cndmask_b32_e64 v29, v95, v18, s[34:35]
	ds_bpermute_b32 v29, v112, v29
	v_cndmask_b32_e64 v18, v18, v95, s[34:35]
	s_waitcnt lgkmcnt(1)
	v_add_f32_e32 v28, v30, v28
	v_cndmask_b32_e64 v30, v96, v19, s[34:35]
	s_waitcnt lgkmcnt(0)
	v_add_f32_e32 v18, v18, v29
	ds_bpermute_b32 v29, v112, v30
	v_cndmask_b32_e64 v19, v19, v96, s[34:35]
	s_waitcnt lgkmcnt(0)
	v_add_f32_e32 v19, v19, v29
	v_cndmask_b32_e64 v29, v2, v23, s[36:37]
	v_cndmask_b32_e64 v2, v23, v2, s[36:37]
	v_cndmask_b32_e64 v23, v4, v24, s[36:37]
	ds_bpermute_b32 v23, v111, v23
	v_cndmask_b32_e64 v4, v24, v4, s[36:37]
	ds_bpermute_b32 v24, v111, v29
	s_waitcnt lgkmcnt(1)
	v_add_f32_e32 v4, v4, v23
	v_cndmask_b32_e64 v23, v5, v25, s[36:37]
	ds_bpermute_b32 v23, v111, v23
	s_waitcnt lgkmcnt(1)
	v_add_f32_e32 v2, v2, v24
	v_cndmask_b32_e64 v5, v25, v5, s[36:37]
	v_cndmask_b32_e64 v24, v6, v26, s[36:37]
	v_cndmask_b32_e64 v6, v26, v6, s[36:37]
	s_waitcnt lgkmcnt(0)
	v_add_f32_e32 v5, v5, v23
	ds_bpermute_b32 v23, v111, v24
	v_cndmask_b32_e64 v24, v20, v28, s[36:37]
	v_cndmask_b32_e64 v20, v28, v20, s[36:37]
	s_waitcnt lgkmcnt(0)
	v_add_f32_e32 v6, v6, v23
	v_cndmask_b32_e64 v23, v7, v27, s[36:37]
	ds_bpermute_b32 v23, v111, v23
	v_cndmask_b32_e64 v7, v27, v7, s[36:37]
	s_waitcnt lgkmcnt(0)
	v_add_f32_e32 v7, v7, v23
	ds_bpermute_b32 v23, v111, v24
	s_waitcnt lgkmcnt(0)
	v_add_f32_e32 v20, v20, v23
	v_cndmask_b32_e64 v23, v21, v18, s[36:37]
	v_cndmask_b32_e64 v18, v18, v21, s[36:37]
	v_cndmask_b32_e64 v21, v22, v19, s[36:37]
	ds_bpermute_b32 v21, v111, v21
	v_cndmask_b32_e64 v19, v19, v22, s[36:37]
	ds_bpermute_b32 v22, v111, v23
	s_waitcnt lgkmcnt(1)
	v_add_f32_e32 v19, v19, v21
	v_cndmask_b32_e64 v21, v2, v7, s[38:39]
	v_cndmask_b32_e64 v2, v7, v2, s[38:39]
	v_cndmask_b32_e64 v7, v4, v20, s[38:39]
	ds_bpermute_b32 v7, v113, v7
	s_waitcnt lgkmcnt(1)
	v_add_f32_e32 v18, v18, v22
	v_cndmask_b32_e64 v4, v20, v4, s[38:39]
	ds_bpermute_b32 v20, v113, v21
	s_waitcnt lgkmcnt(1)
	v_add_f32_e32 v4, v4, v7
	v_cndmask_b32_e64 v7, v5, v18, s[38:39]
	ds_bpermute_b32 v7, v113, v7
	v_cndmask_b32_e64 v5, v18, v5, s[38:39]
	v_cndmask_b32_e64 v18, v6, v19, s[38:39]
	s_waitcnt lgkmcnt(1)
	v_add_f32_e32 v2, v2, v20
	v_cndmask_b32_e64 v6, v19, v6, s[38:39]
	s_waitcnt lgkmcnt(0)
	v_add_f32_e32 v5, v5, v7
	ds_bpermute_b32 v7, v113, v18
	s_waitcnt lgkmcnt(0)
	v_add_f32_e32 v6, v6, v7
	v_cndmask_b32_e64 v7, v2, v5, s[40:41]
	v_cndmask_b32_e64 v2, v5, v2, s[40:41]
	v_cndmask_b32_e64 v5, v4, v6, s[40:41]
	v_cndmask_b32_e64 v4, v6, v4, s[40:41]
	ds_bpermute_b32 v6, v114, v7
	ds_bpermute_b32 v5, v114, v5
	s_waitcnt lgkmcnt(1)
	v_add_f32_e32 v2, v2, v6
	s_waitcnt lgkmcnt(0)
	v_add_f32_e32 v4, v4, v5
	ds_bpermute_b32 v5, v115, v2
	s_waitcnt lgkmcnt(0)
	v_add_f32_e32 v2, v2, v5
	ds_bpermute_b32 v5, v115, v4
	s_waitcnt lgkmcnt(0)
	v_add_f32_e32 v4, v4, v5
	ds_bpermute_b32 v5, v116, v2
	s_waitcnt lgkmcnt(0)
	v_add_f32_e32 v2, v2, v5
	ds_bpermute_b32 v5, v116, v4
	s_waitcnt lgkmcnt(0)
	v_add_f32_e32 v5, v4, v5
	ds_bpermute_b32 v4, v114, v2
	ds_bpermute_b32 v6, v114, v5
	s_waitcnt lgkmcnt(1)
	v_max_f32_e32 v4, v4, v4
	v_max_f32_e32 v4, v2, v4
	ds_bpermute_b32 v7, v113, v4
	s_waitcnt lgkmcnt(1)
	v_max_f32_e32 v6, v6, v6
	v_max_f32_e32 v6, v5, v6
	s_waitcnt lgkmcnt(0)
	v_max_f32_e32 v7, v7, v7
	v_max_f32_e32 v4, v4, v7
	ds_bpermute_b32 v7, v113, v6
	s_waitcnt lgkmcnt(0)
	v_max_f32_e32 v7, v7, v7
	v_max_f32_e32 v6, v6, v7
	ds_bpermute_b32 v7, v111, v4
	s_waitcnt lgkmcnt(0)
	v_max_f32_e32 v7, v7, v7
	v_max_f32_e32 v4, v4, v7
	ds_bpermute_b32 v7, v111, v6
	s_waitcnt lgkmcnt(0)
	v_max_f32_e32 v7, v7, v7
	v_max_f32_e32 v6, v6, v7
	ds_bpermute_b32 v7, v112, v4
	s_waitcnt lgkmcnt(0)
	v_max_f32_e32 v7, v7, v7
	v_max_f32_e32 v4, v4, v7
	ds_bpermute_b32 v7, v112, v6
	v_sub_f32_e32 v2, v2, v4
	v_mul_f32_e32 v2, 0x3fb8aa3b, v2
	v_exp_f32_e32 v4, v2
	s_waitcnt lgkmcnt(0)
	v_max_f32_e32 v7, v7, v7
	v_max_f32_e32 v6, v6, v7
	v_sub_f32_e32 v2, v5, v6
	v_mul_f32_e32 v2, 0x3fb8aa3b, v2
	ds_bpermute_b32 v5, v114, v4
	v_exp_f32_e32 v2, v2
	s_waitcnt lgkmcnt(0)
	v_add_f32_e32 v5, v4, v5
	ds_bpermute_b32 v6, v114, v2
	ds_bpermute_b32 v7, v113, v5
	s_waitcnt lgkmcnt(1)
	v_add_f32_e32 v6, v2, v6
	s_waitcnt lgkmcnt(0)
	v_add_f32_e32 v5, v5, v7
	ds_bpermute_b32 v7, v113, v6
	s_waitcnt lgkmcnt(0)
	v_add_f32_e32 v6, v6, v7
	ds_bpermute_b32 v7, v111, v5
	s_waitcnt lgkmcnt(0)
	v_add_f32_e32 v7, v5, v7
	ds_bpermute_b32 v5, v111, v6
	ds_bpermute_b32 v18, v112, v7
	s_waitcnt lgkmcnt(1)
	v_add_f32_e32 v5, v6, v5
	ds_bpermute_b32 v6, v112, v5
	s_and_saveexec_b64 s[0:1], s[42:43]
	s_cbranch_execz .LBB0_2122
	s_waitcnt lgkmcnt(1)
	v_add_f32_e32 v7, v7, v18
	v_div_scale_f32 v18, s[2:3], v7, v7, v4
	v_rcp_f32_e32 v19, v18
	v_div_scale_f32 v20, vcc, v4, v7, v4
	s_cmp_eq_u32 s8, s48
	v_fma_f32 v21, -v18, v19, 1.0
	v_fmac_f32_e32 v19, v21, v19
	v_mul_f32_e32 v21, v20, v19
	v_fma_f32 v22, -v18, v21, v20
	v_fmac_f32_e32 v21, v22, v19
	v_fma_f32 v18, -v18, v21, v20
	v_div_fmas_f32 v18, v18, v19, v21
	v_div_fixup_f32 v4, v18, v7, v4
	v_lshl_add_u64 v[18:19], s[44:45], 0, v[14:15]
	global_store_dword v[18:19], v4, off
	s_cbranch_scc1 .LBB0_2122
	s_waitcnt lgkmcnt(0)
	v_add_f32_e32 v4, v5, v6
	v_div_scale_f32 v5, s[2:3], v4, v4, v2
	v_rcp_f32_e32 v6, v5
	v_div_scale_f32 v7, vcc, v2, v4, v2
	s_lshl_b64 s[2:3], s[48:49], 6
	v_fma_f32 v18, -v5, v6, 1.0
	v_fmac_f32_e32 v6, v18, v6
	v_mul_f32_e32 v18, v7, v6
	v_fma_f32 v19, -v5, v18, v7
	v_fmac_f32_e32 v18, v19, v6
	v_fma_f32 v5, -v5, v18, v7
	v_div_fmas_f32 v5, v5, v6, v18
	v_div_fixup_f32 v2, v5, v4, v2
	v_lshl_add_u64 v[4:5], v[10:11], 0, s[2:3]
	global_store_dword v[4:5], v2, off
	s_branch .LBB0_2122
